# accumulator clearing at each GEMM unit start and the residual-epilogue buffer copies use packed 64-bit moves (v_pk_mov_b32) instead of pairs of v_mov_b32
# speedup vs baseline: 1.0140x; 1.0140x over previous
.LBB0_177:
	s_ashr_i32 s17, s16, 31
	s_lshl_b64 s[18:19], s[16:17], 20
	s_add_u32 s18, s50, s18
	s_addc_u32 s19, s51, s19
	s_and_b64 s[20:21], s[4:5], exec
	s_cselect_b32 s17, s19, s25
	s_cselect_b32 s54, s18, s24
	s_ashr_i32 s15, s14, 31
	s_lshl_b64 s[20:21], s[14:15], 20
	s_add_u32 s20, s3, s20
	s_addc_u32 s21, s30, s21
	s_and_b64 s[28:29], s[4:5], exec
	s_cselect_b32 s15, s21, s27
	s_cselect_b32 s55, s20, s26
	s_add_u32 s24, s24, 0x80080
	s_addc_u32 s25, s25, 0
	s_add_u32 s56, s26, 0x100
	v_mov_b32_e32 v2, 0
	s_addc_u32 s57, s27, 0
	s_mov_b32 s58, -2
	v_mov_b32_e32 v3, v2
	v_pk_mov_b32 v[4:5], v[2:3], v[2:3]
	v_pk_mov_b32 v[6:7], v[2:3], v[2:3]
	v_pk_mov_b32 v[8:9], v[2:3], v[2:3]
	v_pk_mov_b32 v[10:11], v[2:3], v[2:3]
	v_pk_mov_b32 v[12:13], v[2:3], v[2:3]
	v_pk_mov_b32 v[14:15], v[2:3], v[2:3]
	v_pk_mov_b32 v[16:17], v[2:3], v[2:3]
	v_pk_mov_b32 v[18:19], v[2:3], v[2:3]
	v_pk_mov_b32 v[20:21], v[2:3], v[2:3]
	v_pk_mov_b32 v[22:23], v[2:3], v[2:3]
	v_pk_mov_b32 v[24:25], v[2:3], v[2:3]
	v_pk_mov_b32 v[26:27], v[2:3], v[2:3]
	v_pk_mov_b32 v[28:29], v[2:3], v[2:3]
	v_pk_mov_b32 v[30:31], v[2:3], v[2:3]
	v_pk_mov_b32 v[32:33], v[2:3], v[2:3]
	v_pk_mov_b32 v[34:35], v[2:3], v[2:3]
	v_pk_mov_b32 v[36:37], v[2:3], v[2:3]
	v_pk_mov_b32 v[38:39], v[2:3], v[2:3]
	v_pk_mov_b32 v[40:41], v[2:3], v[2:3]
	v_pk_mov_b32 v[42:43], v[2:3], v[2:3]
	v_pk_mov_b32 v[44:45], v[2:3], v[2:3]
	v_pk_mov_b32 v[46:47], v[2:3], v[2:3]
	v_pk_mov_b32 v[48:49], v[2:3], v[2:3]
	v_pk_mov_b32 v[50:51], v[2:3], v[2:3]
	v_pk_mov_b32 v[52:53], v[2:3], v[2:3]
	v_pk_mov_b32 v[54:55], v[2:3], v[2:3]
	v_pk_mov_b32 v[56:57], v[2:3], v[2:3]
	v_pk_mov_b32 v[58:59], v[2:3], v[2:3]
	v_pk_mov_b32 v[60:61], v[2:3], v[2:3]
	v_pk_mov_b32 v[62:63], v[2:3], v[2:3]
	v_pk_mov_b32 v[64:65], v[2:3], v[2:3]
	v_pk_mov_b32 v[66:67], v[2:3], v[2:3]
	v_pk_mov_b32 v[68:69], v[2:3], v[2:3]
	v_pk_mov_b32 v[70:71], v[2:3], v[2:3]
	v_pk_mov_b32 v[72:73], v[2:3], v[2:3]
	v_pk_mov_b32 v[74:75], v[2:3], v[2:3]
	v_pk_mov_b32 v[76:77], v[2:3], v[2:3]
	v_pk_mov_b32 v[78:79], v[2:3], v[2:3]
	v_pk_mov_b32 v[80:81], v[2:3], v[2:3]
	v_pk_mov_b32 v[82:83], v[2:3], v[2:3]
	v_pk_mov_b32 v[84:85], v[2:3], v[2:3]
	v_pk_mov_b32 v[86:87], v[2:3], v[2:3]
	v_pk_mov_b32 v[88:89], v[2:3], v[2:3]
	v_pk_mov_b32 v[90:91], v[2:3], v[2:3]
	v_pk_mov_b32 v[92:93], v[2:3], v[2:3]
	v_pk_mov_b32 v[94:95], v[2:3], v[2:3]
	v_pk_mov_b32 v[96:97], v[2:3], v[2:3]
	v_pk_mov_b32 v[98:99], v[2:3], v[2:3]
	v_pk_mov_b32 v[100:101], v[2:3], v[2:3]
	v_pk_mov_b32 v[102:103], v[2:3], v[2:3]
	v_pk_mov_b32 v[104:105], v[2:3], v[2:3]
	v_pk_mov_b32 v[106:107], v[2:3], v[2:3]
	v_pk_mov_b32 v[108:109], v[2:3], v[2:3]
	v_pk_mov_b32 v[110:111], v[2:3], v[2:3]
	v_pk_mov_b32 v[112:113], v[2:3], v[2:3]
	v_pk_mov_b32 v[114:115], v[2:3], v[2:3]
	v_pk_mov_b32 v[116:117], v[2:3], v[2:3]
	v_pk_mov_b32 v[118:119], v[2:3], v[2:3]
	v_pk_mov_b32 v[120:121], v[2:3], v[2:3]
	v_pk_mov_b32 v[122:123], v[2:3], v[2:3]
	v_pk_mov_b32 v[124:125], v[2:3], v[2:3]
	v_pk_mov_b32 v[126:127], v[2:3], v[2:3]
	v_pk_mov_b32 v[128:129], v[2:3], v[2:3]

.LBB0_383:
	s_ashr_i32 s19, s18, 31
	s_lshl_b64 s[20:21], s[18:19], 20
	s_add_u32 s20, s70, s20
	s_addc_u32 s21, s71, s21
	s_and_b64 s[22:23], s[6:7], exec
	s_cselect_b32 s19, s21, s29
	s_cselect_b32 s25, s20, s28
	s_ashr_i32 s17, s16, 31
	s_lshl_b64 s[22:23], s[16:17], 20
	s_add_u32 s22, s3, s22
	s_addc_u32 s23, s33, s23
	s_and_b64 s[34:35], s[6:7], exec
	s_cselect_b32 s17, s23, s31
	s_cselect_b32 s56, s22, s30
	s_add_u32 s28, s28, 0x80080
	s_addc_u32 s29, s29, 0
	s_add_u32 s57, s30, 0x100
	v_mov_b32_e32 v2, 0
	s_addc_u32 s58, s31, 0
	s_mov_b32 s59, -2
	s_waitcnt lgkmcnt(0)
	v_mov_b32_e32 v3, v2
	v_pk_mov_b32 v[4:5], v[2:3], v[2:3]
	v_pk_mov_b32 v[6:7], v[2:3], v[2:3]
	v_pk_mov_b32 v[8:9], v[2:3], v[2:3]
	v_pk_mov_b32 v[10:11], v[2:3], v[2:3]
	v_pk_mov_b32 v[12:13], v[2:3], v[2:3]
	v_pk_mov_b32 v[14:15], v[2:3], v[2:3]
	v_pk_mov_b32 v[16:17], v[2:3], v[2:3]
	v_pk_mov_b32 v[18:19], v[2:3], v[2:3]
	v_pk_mov_b32 v[20:21], v[2:3], v[2:3]
	v_pk_mov_b32 v[22:23], v[2:3], v[2:3]
	v_pk_mov_b32 v[24:25], v[2:3], v[2:3]
	v_pk_mov_b32 v[26:27], v[2:3], v[2:3]
	v_pk_mov_b32 v[28:29], v[2:3], v[2:3]
	v_pk_mov_b32 v[30:31], v[2:3], v[2:3]
	v_pk_mov_b32 v[32:33], v[2:3], v[2:3]
	v_pk_mov_b32 v[34:35], v[2:3], v[2:3]
	v_pk_mov_b32 v[36:37], v[2:3], v[2:3]
	v_pk_mov_b32 v[38:39], v[2:3], v[2:3]
	v_pk_mov_b32 v[40:41], v[2:3], v[2:3]
	v_pk_mov_b32 v[42:43], v[2:3], v[2:3]
	v_pk_mov_b32 v[44:45], v[2:3], v[2:3]
	v_pk_mov_b32 v[46:47], v[2:3], v[2:3]
	v_pk_mov_b32 v[48:49], v[2:3], v[2:3]
	v_pk_mov_b32 v[50:51], v[2:3], v[2:3]
	v_pk_mov_b32 v[52:53], v[2:3], v[2:3]
	v_pk_mov_b32 v[54:55], v[2:3], v[2:3]
	v_pk_mov_b32 v[56:57], v[2:3], v[2:3]
	v_pk_mov_b32 v[58:59], v[2:3], v[2:3]
	v_pk_mov_b32 v[60:61], v[2:3], v[2:3]
	v_pk_mov_b32 v[62:63], v[2:3], v[2:3]
	v_pk_mov_b32 v[64:65], v[2:3], v[2:3]
	v_pk_mov_b32 v[66:67], v[2:3], v[2:3]
	v_pk_mov_b32 v[68:69], v[2:3], v[2:3]
	v_pk_mov_b32 v[70:71], v[2:3], v[2:3]
	v_pk_mov_b32 v[72:73], v[2:3], v[2:3]
	v_pk_mov_b32 v[74:75], v[2:3], v[2:3]
	v_pk_mov_b32 v[76:77], v[2:3], v[2:3]
	v_pk_mov_b32 v[78:79], v[2:3], v[2:3]
	v_pk_mov_b32 v[80:81], v[2:3], v[2:3]
	v_pk_mov_b32 v[82:83], v[2:3], v[2:3]
	v_pk_mov_b32 v[84:85], v[2:3], v[2:3]
	v_pk_mov_b32 v[86:87], v[2:3], v[2:3]
	v_pk_mov_b32 v[88:89], v[2:3], v[2:3]
	v_pk_mov_b32 v[90:91], v[2:3], v[2:3]
	v_pk_mov_b32 v[92:93], v[2:3], v[2:3]
	v_pk_mov_b32 v[94:95], v[2:3], v[2:3]
	v_pk_mov_b32 v[96:97], v[2:3], v[2:3]
	v_pk_mov_b32 v[98:99], v[2:3], v[2:3]
	v_pk_mov_b32 v[100:101], v[2:3], v[2:3]
	v_pk_mov_b32 v[102:103], v[2:3], v[2:3]
	v_pk_mov_b32 v[104:105], v[2:3], v[2:3]
	v_pk_mov_b32 v[106:107], v[2:3], v[2:3]
	v_pk_mov_b32 v[108:109], v[2:3], v[2:3]
	v_pk_mov_b32 v[110:111], v[2:3], v[2:3]
	v_pk_mov_b32 v[112:113], v[2:3], v[2:3]
	v_pk_mov_b32 v[114:115], v[2:3], v[2:3]
	v_pk_mov_b32 v[116:117], v[2:3], v[2:3]
	v_pk_mov_b32 v[118:119], v[2:3], v[2:3]
	v_pk_mov_b32 v[120:121], v[2:3], v[2:3]
	v_pk_mov_b32 v[122:123], v[2:3], v[2:3]
	v_pk_mov_b32 v[124:125], v[2:3], v[2:3]
	v_pk_mov_b32 v[126:127], v[2:3], v[2:3]
	v_pk_mov_b32 v[128:129], v[2:3], v[2:3]

.LBB0_387:
	v_lshl_add_u32 v150, s24, 8, v152
	v_lshl_or_b32 v148, s26, 8, v154
	v_ashrrev_i32_e32 v151, 31, v150
	v_ashrrev_i32_e32 v149, 31, v148
	v_lshlrev_b64 v[160:161], 11, v[150:151]
	v_lshl_add_u64 v[168:169], v[160:161], 0, v[148:149]
	v_lshl_add_u64 v[170:171], v[168:169], 2, s[48:49]
	v_mov_b32_e32 v222, v170
	v_mov_b32_e32 v223, v171
	v_mov_b32_e32 v240, 0x20000
	v_mov_b32_e32 v241, 0
	global_load_dwordx4 v[174:177], v[222:223], off
	global_load_dwordx4 v[178:181], v[222:223], off offset:16
	global_load_dwordx4 v[182:185], v[222:223], off offset:512
	global_load_dwordx4 v[190:193], v[222:223], off offset:528
	v_lshl_add_u64 v[222:223], v[240:241], 0, v[222:223]
	global_load_dwordx4 v[194:197], v[222:223], off
	global_load_dwordx4 v[198:201], v[222:223], off offset:16
	global_load_dwordx4 v[202:205], v[222:223], off offset:512
	global_load_dwordx4 v[206:209], v[222:223], off offset:528
	v_lshl_add_u64 v[222:223], v[240:241], 0, v[222:223]
	global_load_dwordx4 v[210:213], v[222:223], off
	global_load_dwordx4 v[214:217], v[222:223], off offset:16
	global_load_dwordx4 v[218:221], v[222:223], off offset:512
	global_load_dwordx4 v[228:231], v[222:223], off offset:528
	s_nop 0
	s_nop 0
	v_lshl_add_u64 v[168:169], v[168:169], 1, s[50:51]
	s_waitcnt vmcnt(8)
	s_nop 1
	v_pk_mov_b32 v[160:161], v[174:175], v[174:175] op_sel:[0,1]
	v_pk_mov_b32 v[162:163], v[176:177], v[176:177] op_sel:[0,1]
	v_pk_mov_b32 v[164:165], v[178:179], v[178:179] op_sel:[0,1]
	v_pk_mov_b32 v[166:167], v[180:181], v[180:181] op_sel:[0,1]
	v_pk_add_f32 v[128:129], v[128:129], v[162:163]
	v_pk_add_f32 v[172:173], v[126:127], v[160:161]
	v_pk_add_f32 v[166:167], v[124:125], v[166:167]
	v_pk_add_f32 v[164:165], v[122:123], v[164:165]
	v_cvt_pk_bf16_f32 v122, v172, v173
	v_cvt_pk_bf16_f32 v123, v128, v129
	v_mul_f32_e32 v129, v129, v129
	v_cvt_pk_bf16_f32 v124, v164, v165
	v_cvt_pk_bf16_f32 v125, v166, v167
	global_store_dwordx4 v[168:169], v[122:125], off
	s_nop 0
	s_nop 0
	s_nop 0
	v_and_b32_e32 v123, 64, v159
	v_mul_f32_e32 v170, v173, v173
	v_mul_f32_e32 v165, v165, v165
	v_mul_f32_e32 v167, v167, v167
	v_xor_b32_e32 v122, 16, v159
	v_add_u32_e32 v123, 64, v123
	v_fmac_f32_e32 v170, v172, v172
	v_fmac_f32_e32 v129, v128, v128
	v_fmac_f32_e32 v165, v164, v164
	v_fmac_f32_e32 v167, v166, v166
	v_cmp_lt_i32_e32 vcc, v122, v123
	v_add_f32_e32 v128, v170, v129
	v_add_f32_e32 v129, v165, v167
	v_cndmask_b32_e32 v122, v159, v122, vcc
	v_add_f32_e32 v128, v128, v129
	v_lshlrev_b32_e32 v122, 2, v122
	s_nop 1
	v_pk_mov_b32 v[124:125], v[182:183], v[182:183] op_sel:[0,1]
	v_pk_mov_b32 v[126:127], v[184:185], v[184:185] op_sel:[0,1]
	v_pk_add_f32 v[120:121], v[120:121], v[126:127]
	v_pk_add_f32 v[118:119], v[118:119], v[124:125]
	s_nop 1
	v_pk_mov_b32 v[160:161], v[190:191], v[190:191] op_sel:[0,1]
	v_pk_mov_b32 v[162:163], v[192:193], v[192:193] op_sel:[0,1]
	v_lshl_add_u64 v[222:223], v[240:241], 0, v[222:223]
	global_load_dwordx4 v[174:177], v[222:223], off
	global_load_dwordx4 v[178:181], v[222:223], off offset:16
	global_load_dwordx4 v[182:185], v[222:223], off offset:512
	global_load_dwordx4 v[190:193], v[222:223], off offset:528
	v_pk_add_f32 v[124:125], v[116:117], v[162:163]
	v_pk_add_f32 v[126:127], v[114:115], v[160:161]
	v_mul_f32_e32 v114, v119, v119
	v_mul_f32_e32 v115, v121, v121
	v_mul_f32_e32 v116, v127, v127
	v_mul_f32_e32 v117, v125, v125
	v_fmac_f32_e32 v114, v118, v118
	v_fmac_f32_e32 v115, v120, v120
	v_fmac_f32_e32 v116, v126, v126
	v_fmac_f32_e32 v117, v124, v124
	v_add_f32_e32 v114, v114, v115
	v_add_f32_e32 v115, v116, v117
	v_add_f32_e32 v114, v114, v115
	v_add_f32_e32 v114, v128, v114
	ds_bpermute_b32 v115, v122, v114
	v_xor_b32_e32 v116, 32, v159
	v_cmp_lt_i32_e32 vcc, v116, v123
	v_cvt_pk_bf16_f32 v118, v118, v119
	v_cvt_pk_bf16_f32 v119, v120, v121
	s_waitcnt lgkmcnt(0)
	v_add_f32_e32 v114, v114, v115
	v_cvt_pk_bf16_f32 v120, v126, v127
	v_cvt_pk_bf16_f32 v121, v124, v125
	v_cndmask_b32_e32 v116, v159, v116, vcc
	v_lshlrev_b32_e32 v116, 2, v116
	ds_bpermute_b32 v115, v116, v114
	global_store_dwordx4 v[168:169], v[118:121], off offset:256
	s_and_saveexec_b64 s[24:25], s[4:5]
	s_cbranch_execz .LBB0_389
	s_waitcnt lgkmcnt(0)
	v_add_f32_e32 v114, v114, v115
	v_fma_f32 v114, v114, s55, 0.5
	v_trunc_f32_e32 v114, v114
	v_mul_f32_e32 v115, 0x2f800000, v114
	v_floor_f32_e32 v115, v115
	v_fmac_f32_e32 v114, 0xcf800000, v115
	v_cvt_u32_f32_e32 v114, v114
	v_cvt_u32_f32_e32 v115, v115
	v_lshl_add_u64 v[118:119], v[150:151], 3, s[10:11]
	global_atomic_add_x2 v[118:119], v[114:115], off
.LBB0_389:
	s_or_b64 exec, exec, s[24:25]
	v_or_b32_e32 v114, 16, v150
	s_waitcnt lgkmcnt(0)
	v_ashrrev_i32_e32 v115, 31, v114
	v_lshlrev_b64 v[118:119], 11, v[114:115]
	v_lshl_add_u64 v[128:129], v[118:119], 0, v[148:149]
	v_lshl_add_u64 v[160:161], v[128:129], 2, s[48:49]
	s_nop 0
	s_nop 0
	v_lshl_add_u64 v[128:129], v[128:129], 1, s[50:51]
	s_waitcnt vmcnt(10)
	s_nop 1
	v_pk_mov_b32 v[118:119], v[194:195], v[194:195] op_sel:[0,1]
	v_pk_mov_b32 v[120:121], v[196:197], v[196:197] op_sel:[0,1]
	v_pk_add_f32 v[120:121], v[112:113], v[120:121]
	v_pk_add_f32 v[118:119], v[110:111], v[118:119]
	s_nop 1
	v_pk_mov_b32 v[124:125], v[198:199], v[198:199] op_sel:[0,1]
	v_pk_mov_b32 v[126:127], v[200:201], v[200:201] op_sel:[0,1]
	v_pk_add_f32 v[126:127], v[108:109], v[126:127]
	v_pk_add_f32 v[124:125], v[106:107], v[124:125]
	v_cvt_pk_bf16_f32 v106, v118, v119
	v_cvt_pk_bf16_f32 v107, v120, v121
	v_mul_f32_e32 v117, v119, v119
	v_cvt_pk_bf16_f32 v108, v124, v125
	v_cvt_pk_bf16_f32 v109, v126, v127
	global_store_dwordx4 v[128:129], v[106:109], off
	s_nop 0
	s_nop 0
	s_nop 0
	v_mul_f32_e32 v119, v121, v121
	v_mul_f32_e32 v121, v125, v125
	v_mul_f32_e32 v123, v127, v127
	v_fmac_f32_e32 v117, v118, v118
	v_fmac_f32_e32 v119, v120, v120
	v_fmac_f32_e32 v121, v124, v124
	v_fmac_f32_e32 v123, v126, v126
	v_add_f32_e32 v117, v117, v119
	v_add_f32_e32 v118, v121, v123
	v_add_f32_e32 v117, v117, v118
	s_nop 1
	v_pk_mov_b32 v[106:107], v[202:203], v[202:203] op_sel:[0,1]
	v_pk_mov_b32 v[108:109], v[204:205], v[204:205] op_sel:[0,1]
	v_pk_add_f32 v[104:105], v[104:105], v[108:109]
	v_pk_add_f32 v[102:103], v[102:103], v[106:107]
	s_nop 1
	v_pk_mov_b32 v[110:111], v[206:207], v[206:207] op_sel:[0,1]
	v_pk_mov_b32 v[112:113], v[208:209], v[208:209] op_sel:[0,1]
	v_lshl_add_u64 v[222:223], v[240:241], 2, v[222:223]
	v_lshl_add_u64 v[222:223], v[240:241], 0, v[222:223]
	global_load_dwordx4 v[194:197], v[222:223], off
	global_load_dwordx4 v[198:201], v[222:223], off offset:16
	global_load_dwordx4 v[202:205], v[222:223], off offset:512
	global_load_dwordx4 v[206:209], v[222:223], off offset:528
	v_pk_add_f32 v[106:107], v[100:101], v[112:113]
	v_pk_add_f32 v[108:109], v[98:99], v[110:111]
	v_mul_f32_e32 v98, v103, v103
	v_mul_f32_e32 v99, v105, v105
	v_mul_f32_e32 v100, v109, v109
	v_mul_f32_e32 v101, v107, v107
	v_fmac_f32_e32 v98, v102, v102
	v_fmac_f32_e32 v99, v104, v104
	v_fmac_f32_e32 v100, v108, v108
	v_fmac_f32_e32 v101, v106, v106
	v_add_f32_e32 v98, v98, v99
	v_add_f32_e32 v99, v100, v101
	v_add_f32_e32 v98, v98, v99
	v_add_f32_e32 v98, v117, v98
	ds_bpermute_b32 v99, v122, v98
	v_cvt_pk_bf16_f32 v100, v102, v103
	v_cvt_pk_bf16_f32 v101, v104, v105
	v_cvt_pk_bf16_f32 v102, v108, v109
	v_cvt_pk_bf16_f32 v103, v106, v107
	s_waitcnt lgkmcnt(0)
	v_add_f32_e32 v98, v98, v99
	ds_bpermute_b32 v99, v116, v98
	global_store_dwordx4 v[128:129], v[100:103], off offset:256
	s_and_saveexec_b64 s[24:25], s[4:5]
	s_cbranch_execz .LBB0_391
	s_waitcnt lgkmcnt(0)
	v_add_f32_e32 v98, v98, v99
	v_fma_f32 v98, v98, s55, 0.5
	v_trunc_f32_e32 v98, v98
	v_mul_f32_e32 v99, 0x2f800000, v98
	v_floor_f32_e32 v99, v99
	v_fmac_f32_e32 v98, 0xcf800000, v99
	v_cvt_u32_f32_e32 v98, v98
	v_cvt_u32_f32_e32 v99, v99
	v_lshl_add_u64 v[100:101], v[114:115], 3, s[10:11]
	global_atomic_add_x2 v[100:101], v[98:99], off
.LBB0_391:
	s_or_b64 exec, exec, s[24:25]
	v_or_b32_e32 v98, 32, v150
	s_waitcnt lgkmcnt(0)
	v_ashrrev_i32_e32 v99, 31, v98
	v_lshlrev_b64 v[100:101], 11, v[98:99]
	v_lshl_add_u64 v[108:109], v[100:101], 0, v[148:149]
	v_lshl_add_u64 v[110:111], v[108:109], 2, s[48:49]
	s_nop 0
	s_nop 0
	v_lshl_add_u64 v[108:109], v[108:109], 1, s[50:51]
	s_waitcnt vmcnt(12)
	s_nop 1
	v_pk_mov_b32 v[100:101], v[210:211], v[210:211] op_sel:[0,1]
	v_pk_mov_b32 v[102:103], v[212:213], v[212:213] op_sel:[0,1]
	v_pk_add_f32 v[102:103], v[96:97], v[102:103]
	v_pk_add_f32 v[100:101], v[94:95], v[100:101]
	s_nop 1
	v_pk_mov_b32 v[104:105], v[214:215], v[214:215] op_sel:[0,1]
	v_pk_mov_b32 v[106:107], v[216:217], v[216:217] op_sel:[0,1]
	v_pk_add_f32 v[106:107], v[92:93], v[106:107]
	v_pk_add_f32 v[104:105], v[90:91], v[104:105]
	v_cvt_pk_bf16_f32 v90, v100, v101
	v_cvt_pk_bf16_f32 v91, v102, v103
	v_mul_f32_e32 v101, v101, v101
	v_cvt_pk_bf16_f32 v92, v104, v105
	v_cvt_pk_bf16_f32 v93, v106, v107
	global_store_dwordx4 v[108:109], v[90:93], off
	s_nop 0
	s_nop 0
	s_nop 0
	v_mul_f32_e32 v103, v103, v103
	v_mul_f32_e32 v105, v105, v105
	v_mul_f32_e32 v107, v107, v107
	v_fmac_f32_e32 v101, v100, v100
	v_fmac_f32_e32 v103, v102, v102
	v_fmac_f32_e32 v105, v104, v104
	v_fmac_f32_e32 v107, v106, v106
	v_add_f32_e32 v100, v101, v103
	v_add_f32_e32 v101, v105, v107
	v_add_f32_e32 v100, v100, v101
	s_nop 1
	v_pk_mov_b32 v[90:91], v[218:219], v[218:219] op_sel:[0,1]
	v_pk_mov_b32 v[92:93], v[220:221], v[220:221] op_sel:[0,1]
	v_pk_add_f32 v[88:89], v[88:89], v[92:93]
	v_pk_add_f32 v[86:87], v[86:87], v[90:91]
	s_nop 1
	v_pk_mov_b32 v[94:95], v[228:229], v[228:229] op_sel:[0,1]
	v_pk_mov_b32 v[96:97], v[230:231], v[230:231] op_sel:[0,1]
	v_lshl_add_u64 v[222:223], v[240:241], 0, v[222:223]
	global_load_dwordx4 v[210:213], v[222:223], off
	global_load_dwordx4 v[214:217], v[222:223], off offset:16
	global_load_dwordx4 v[218:221], v[222:223], off offset:512
	global_load_dwordx4 v[228:231], v[222:223], off offset:528
	v_pk_add_f32 v[90:91], v[84:85], v[96:97]
	v_pk_add_f32 v[92:93], v[82:83], v[94:95]
	v_mul_f32_e32 v82, v87, v87
	v_mul_f32_e32 v83, v89, v89
	v_mul_f32_e32 v84, v93, v93
	v_mul_f32_e32 v85, v91, v91
	v_fmac_f32_e32 v82, v86, v86
	v_fmac_f32_e32 v83, v88, v88
	v_fmac_f32_e32 v84, v92, v92
	v_fmac_f32_e32 v85, v90, v90
	v_add_f32_e32 v82, v82, v83
	v_add_f32_e32 v83, v84, v85
	v_add_f32_e32 v82, v82, v83
	v_add_f32_e32 v82, v100, v82
	ds_bpermute_b32 v83, v122, v82
	v_cvt_pk_bf16_f32 v84, v86, v87
	v_cvt_pk_bf16_f32 v85, v88, v89
	v_cvt_pk_bf16_f32 v86, v92, v93
	v_cvt_pk_bf16_f32 v87, v90, v91
	s_waitcnt lgkmcnt(0)
	v_add_f32_e32 v82, v82, v83
	ds_bpermute_b32 v83, v116, v82
	global_store_dwordx4 v[108:109], v[84:87], off offset:256
	s_and_saveexec_b64 s[24:25], s[4:5]
	s_cbranch_execz .LBB0_393
	s_waitcnt lgkmcnt(0)
	v_add_f32_e32 v82, v82, v83
	v_fma_f32 v82, v82, s55, 0.5
	v_trunc_f32_e32 v82, v82
	v_mul_f32_e32 v83, 0x2f800000, v82
	v_floor_f32_e32 v83, v83
	v_fmac_f32_e32 v82, 0xcf800000, v83
	v_cvt_u32_f32_e32 v82, v82
	v_cvt_u32_f32_e32 v83, v83
	v_lshl_add_u64 v[84:85], v[98:99], 3, s[10:11]
	global_atomic_add_x2 v[84:85], v[82:83], off
.LBB0_393:
	s_or_b64 exec, exec, s[24:25]
	v_or_b32_e32 v82, 48, v150
	s_waitcnt lgkmcnt(0)
	v_ashrrev_i32_e32 v83, 31, v82
	v_lshlrev_b64 v[84:85], 11, v[82:83]
	v_lshl_add_u64 v[92:93], v[84:85], 0, v[148:149]
	v_lshl_add_u64 v[94:95], v[92:93], 2, s[48:49]
	s_nop 0
	s_nop 0
	v_lshl_add_u64 v[92:93], v[92:93], 1, s[50:51]
	s_waitcnt vmcnt(13)
	s_nop 1
	v_pk_mov_b32 v[84:85], v[174:175], v[174:175] op_sel:[0,1]
	v_pk_mov_b32 v[86:87], v[176:177], v[176:177] op_sel:[0,1]
	v_pk_add_f32 v[86:87], v[80:81], v[86:87]
	v_pk_add_f32 v[84:85], v[78:79], v[84:85]
	s_nop 1
	v_pk_mov_b32 v[88:89], v[178:179], v[178:179] op_sel:[0,1]
	v_pk_mov_b32 v[90:91], v[180:181], v[180:181] op_sel:[0,1]
	v_pk_add_f32 v[90:91], v[76:77], v[90:91]
	v_pk_add_f32 v[88:89], v[74:75], v[88:89]
	v_cvt_pk_bf16_f32 v74, v84, v85
	v_cvt_pk_bf16_f32 v75, v86, v87
	v_mul_f32_e32 v85, v85, v85
	v_cvt_pk_bf16_f32 v76, v88, v89
	v_cvt_pk_bf16_f32 v77, v90, v91
	global_store_dwordx4 v[92:93], v[74:77], off
	s_nop 0
	s_nop 0
	s_nop 0
	v_mul_f32_e32 v87, v87, v87
	v_mul_f32_e32 v89, v89, v89
	v_mul_f32_e32 v91, v91, v91
	v_fmac_f32_e32 v85, v84, v84
	v_fmac_f32_e32 v87, v86, v86
	v_fmac_f32_e32 v89, v88, v88
	v_fmac_f32_e32 v91, v90, v90
	v_add_f32_e32 v84, v85, v87
	v_add_f32_e32 v85, v89, v91
	v_add_f32_e32 v84, v84, v85
	s_nop 1
	v_pk_mov_b32 v[74:75], v[182:183], v[182:183] op_sel:[0,1]
	v_pk_mov_b32 v[76:77], v[184:185], v[184:185] op_sel:[0,1]
	v_pk_add_f32 v[72:73], v[72:73], v[76:77]
	v_pk_add_f32 v[70:71], v[70:71], v[74:75]
	s_nop 1
	v_pk_mov_b32 v[78:79], v[190:191], v[190:191] op_sel:[0,1]
	v_pk_mov_b32 v[80:81], v[192:193], v[192:193] op_sel:[0,1]
	v_lshl_add_u64 v[222:223], v[240:241], 0, v[222:223]
	global_load_dwordx4 v[174:177], v[222:223], off
	global_load_dwordx4 v[178:181], v[222:223], off offset:16
	global_load_dwordx4 v[182:185], v[222:223], off offset:512
	global_load_dwordx4 v[190:193], v[222:223], off offset:528
	v_pk_add_f32 v[74:75], v[68:69], v[80:81]
	v_pk_add_f32 v[76:77], v[66:67], v[78:79]
	v_mul_f32_e32 v66, v71, v71
	v_mul_f32_e32 v67, v73, v73
	v_mul_f32_e32 v68, v77, v77
	v_mul_f32_e32 v69, v75, v75
	v_fmac_f32_e32 v66, v70, v70
	v_fmac_f32_e32 v67, v72, v72
	v_fmac_f32_e32 v68, v76, v76
	v_fmac_f32_e32 v69, v74, v74
	v_add_f32_e32 v66, v66, v67
	v_add_f32_e32 v67, v68, v69
	v_add_f32_e32 v66, v66, v67
	v_add_f32_e32 v66, v84, v66
	ds_bpermute_b32 v67, v122, v66
	v_cvt_pk_bf16_f32 v68, v70, v71
	v_cvt_pk_bf16_f32 v69, v72, v73
	v_cvt_pk_bf16_f32 v70, v76, v77
	v_cvt_pk_bf16_f32 v71, v74, v75
	s_waitcnt lgkmcnt(0)
	v_add_f32_e32 v66, v66, v67
	ds_bpermute_b32 v67, v116, v66
	global_store_dwordx4 v[92:93], v[68:71], off offset:256
	s_and_saveexec_b64 s[24:25], s[4:5]
	s_cbranch_execz .LBB0_395
	s_waitcnt lgkmcnt(0)
	v_add_f32_e32 v66, v66, v67
	v_fma_f32 v66, v66, s55, 0.5
	v_trunc_f32_e32 v66, v66
	v_mul_f32_e32 v67, 0x2f800000, v66
	v_floor_f32_e32 v67, v67
	v_fmac_f32_e32 v66, 0xcf800000, v67
	v_cvt_u32_f32_e32 v66, v66
	v_cvt_u32_f32_e32 v67, v67
	v_lshl_add_u64 v[68:69], v[82:83], 3, s[10:11]
	global_atomic_add_x2 v[68:69], v[66:67], off
.LBB0_395:
	s_or_b64 exec, exec, s[24:25]
	v_add_u32_e32 v66, 0x80, v150
	s_waitcnt lgkmcnt(0)
	v_ashrrev_i32_e32 v67, 31, v66
	v_lshlrev_b64 v[68:69], 11, v[66:67]
	v_lshl_add_u64 v[76:77], v[68:69], 0, v[148:149]
	v_lshl_add_u64 v[78:79], v[76:77], 2, s[48:49]
	s_nop 0
	s_nop 0
	v_lshl_add_u64 v[76:77], v[76:77], 1, s[50:51]
	s_waitcnt vmcnt(13)
	s_nop 1
	v_pk_mov_b32 v[68:69], v[194:195], v[194:195] op_sel:[0,1]
	v_pk_mov_b32 v[70:71], v[196:197], v[196:197] op_sel:[0,1]
	v_pk_add_f32 v[70:71], v[64:65], v[70:71]
	v_pk_add_f32 v[68:69], v[62:63], v[68:69]
	s_nop 1
	v_pk_mov_b32 v[72:73], v[198:199], v[198:199] op_sel:[0,1]
	v_pk_mov_b32 v[74:75], v[200:201], v[200:201] op_sel:[0,1]
	v_pk_add_f32 v[74:75], v[60:61], v[74:75]
	v_pk_add_f32 v[72:73], v[58:59], v[72:73]
	v_cvt_pk_bf16_f32 v58, v68, v69
	v_cvt_pk_bf16_f32 v59, v70, v71
	v_mul_f32_e32 v69, v69, v69
	v_cvt_pk_bf16_f32 v60, v72, v73
	v_cvt_pk_bf16_f32 v61, v74, v75
	global_store_dwordx4 v[76:77], v[58:61], off
	s_nop 0
	s_nop 0
	s_nop 0
	v_mul_f32_e32 v71, v71, v71
	v_mul_f32_e32 v73, v73, v73
	v_mul_f32_e32 v75, v75, v75
	v_fmac_f32_e32 v69, v68, v68
	v_fmac_f32_e32 v71, v70, v70
	v_fmac_f32_e32 v73, v72, v72
	v_fmac_f32_e32 v75, v74, v74
	v_add_f32_e32 v68, v69, v71
	v_add_f32_e32 v69, v73, v75
	v_add_f32_e32 v68, v68, v69
	s_nop 1
	v_pk_mov_b32 v[58:59], v[202:203], v[202:203] op_sel:[0,1]
	v_pk_mov_b32 v[60:61], v[204:205], v[204:205] op_sel:[0,1]
	v_pk_add_f32 v[56:57], v[56:57], v[60:61]
	v_pk_add_f32 v[54:55], v[54:55], v[58:59]
	s_nop 1
	v_pk_mov_b32 v[62:63], v[206:207], v[206:207] op_sel:[0,1]
	v_pk_mov_b32 v[64:65], v[208:209], v[208:209] op_sel:[0,1]
	v_lshl_add_u64 v[222:223], v[240:241], 0, v[222:223]
	global_load_dwordx4 v[194:197], v[222:223], off
	global_load_dwordx4 v[198:201], v[222:223], off offset:16
	global_load_dwordx4 v[202:205], v[222:223], off offset:512
	global_load_dwordx4 v[206:209], v[222:223], off offset:528
	v_pk_add_f32 v[58:59], v[52:53], v[64:65]
	v_pk_add_f32 v[60:61], v[50:51], v[62:63]
	v_mul_f32_e32 v50, v55, v55
	v_mul_f32_e32 v51, v57, v57
	v_mul_f32_e32 v52, v61, v61
	v_mul_f32_e32 v53, v59, v59
	v_fmac_f32_e32 v50, v54, v54
	v_fmac_f32_e32 v51, v56, v56
	v_fmac_f32_e32 v52, v60, v60
	v_fmac_f32_e32 v53, v58, v58
	v_add_f32_e32 v50, v50, v51
	v_add_f32_e32 v51, v52, v53
	v_add_f32_e32 v50, v50, v51
	v_add_f32_e32 v50, v68, v50
	ds_bpermute_b32 v51, v122, v50
	v_cvt_pk_bf16_f32 v52, v54, v55
	v_cvt_pk_bf16_f32 v53, v56, v57
	v_cvt_pk_bf16_f32 v54, v60, v61
	v_cvt_pk_bf16_f32 v55, v58, v59
	s_waitcnt lgkmcnt(0)
	v_add_f32_e32 v50, v50, v51
	ds_bpermute_b32 v51, v116, v50
	global_store_dwordx4 v[76:77], v[52:55], off offset:256
	s_and_saveexec_b64 s[24:25], s[4:5]
	s_cbranch_execz .LBB0_397
	s_waitcnt lgkmcnt(0)
	v_add_f32_e32 v50, v50, v51
	v_fma_f32 v50, v50, s55, 0.5
	v_trunc_f32_e32 v50, v50
	v_mul_f32_e32 v51, 0x2f800000, v50
	v_floor_f32_e32 v51, v51
	v_fmac_f32_e32 v50, 0xcf800000, v51
	v_cvt_u32_f32_e32 v50, v50
	v_cvt_u32_f32_e32 v51, v51
	v_lshl_add_u64 v[52:53], v[66:67], 3, s[10:11]
	global_atomic_add_x2 v[52:53], v[50:51], off
.LBB0_397:
	s_or_b64 exec, exec, s[24:25]
	v_add_u32_e32 v50, 0x90, v150
	s_waitcnt lgkmcnt(0)
	v_ashrrev_i32_e32 v51, 31, v50
	v_lshlrev_b64 v[52:53], 11, v[50:51]
	v_lshl_add_u64 v[60:61], v[52:53], 0, v[148:149]
	v_lshl_add_u64 v[62:63], v[60:61], 2, s[48:49]
	s_nop 0
	s_nop 0
	v_lshl_add_u64 v[60:61], v[60:61], 1, s[50:51]
	s_waitcnt vmcnt(13)
	s_nop 1
	v_pk_mov_b32 v[52:53], v[210:211], v[210:211] op_sel:[0,1]
	v_pk_mov_b32 v[54:55], v[212:213], v[212:213] op_sel:[0,1]
	v_pk_add_f32 v[54:55], v[48:49], v[54:55]
	v_pk_add_f32 v[52:53], v[46:47], v[52:53]
	s_nop 1
	v_pk_mov_b32 v[56:57], v[214:215], v[214:215] op_sel:[0,1]
	v_pk_mov_b32 v[58:59], v[216:217], v[216:217] op_sel:[0,1]
	v_pk_add_f32 v[58:59], v[44:45], v[58:59]
	v_pk_add_f32 v[56:57], v[42:43], v[56:57]
	v_cvt_pk_bf16_f32 v42, v52, v53
	v_cvt_pk_bf16_f32 v43, v54, v55
	v_mul_f32_e32 v53, v53, v53
	v_cvt_pk_bf16_f32 v44, v56, v57
	v_cvt_pk_bf16_f32 v45, v58, v59
	global_store_dwordx4 v[60:61], v[42:45], off
	s_nop 0
	s_nop 0
	s_nop 0
	v_mul_f32_e32 v55, v55, v55
	v_mul_f32_e32 v57, v57, v57
	v_mul_f32_e32 v59, v59, v59
	v_fmac_f32_e32 v53, v52, v52
	v_fmac_f32_e32 v55, v54, v54
	v_fmac_f32_e32 v57, v56, v56
	v_fmac_f32_e32 v59, v58, v58
	v_add_f32_e32 v52, v53, v55
	v_add_f32_e32 v53, v57, v59
	v_add_f32_e32 v52, v52, v53
	s_nop 1
	v_pk_mov_b32 v[42:43], v[218:219], v[218:219] op_sel:[0,1]
	v_pk_mov_b32 v[44:45], v[220:221], v[220:221] op_sel:[0,1]
	v_pk_add_f32 v[40:41], v[40:41], v[44:45]
	v_pk_add_f32 v[38:39], v[38:39], v[42:43]
	s_nop 1
	v_pk_mov_b32 v[46:47], v[228:229], v[228:229] op_sel:[0,1]
	v_pk_mov_b32 v[48:49], v[230:231], v[230:231] op_sel:[0,1]
	v_pk_add_f32 v[42:43], v[36:37], v[48:49]
	v_pk_add_f32 v[44:45], v[34:35], v[46:47]
	v_mul_f32_e32 v34, v39, v39
	v_mul_f32_e32 v35, v41, v41
	v_mul_f32_e32 v36, v45, v45
	v_mul_f32_e32 v37, v43, v43
	v_fmac_f32_e32 v34, v38, v38
	v_fmac_f32_e32 v35, v40, v40
	v_fmac_f32_e32 v36, v44, v44
	v_fmac_f32_e32 v37, v42, v42
	v_add_f32_e32 v34, v34, v35
	v_add_f32_e32 v35, v36, v37
	v_add_f32_e32 v34, v34, v35
	v_add_f32_e32 v34, v52, v34
	ds_bpermute_b32 v35, v122, v34
	v_cvt_pk_bf16_f32 v36, v38, v39
	v_cvt_pk_bf16_f32 v37, v40, v41
	v_cvt_pk_bf16_f32 v38, v44, v45
	v_cvt_pk_bf16_f32 v39, v42, v43
	s_waitcnt lgkmcnt(0)
	v_add_f32_e32 v34, v34, v35
	ds_bpermute_b32 v35, v116, v34
	global_store_dwordx4 v[60:61], v[36:39], off offset:256
	s_and_saveexec_b64 s[24:25], s[4:5]
	s_cbranch_execz .LBB0_399
	s_waitcnt lgkmcnt(0)
	v_add_f32_e32 v34, v34, v35
	v_fma_f32 v34, v34, s55, 0.5
	v_trunc_f32_e32 v34, v34
	v_mul_f32_e32 v35, 0x2f800000, v34
	v_floor_f32_e32 v35, v35
	v_fmac_f32_e32 v34, 0xcf800000, v35
	v_cvt_u32_f32_e32 v34, v34
	v_cvt_u32_f32_e32 v35, v35
	v_lshl_add_u64 v[36:37], v[50:51], 3, s[10:11]
	global_atomic_add_x2 v[36:37], v[34:35], off
.LBB0_399:
	s_or_b64 exec, exec, s[24:25]
	v_add_u32_e32 v34, 0xa0, v150
	s_waitcnt lgkmcnt(0)
	v_ashrrev_i32_e32 v35, 31, v34
	v_lshlrev_b64 v[36:37], 11, v[34:35]
	v_lshl_add_u64 v[44:45], v[36:37], 0, v[148:149]
	v_lshl_add_u64 v[46:47], v[44:45], 2, s[48:49]
	s_nop 0
	s_nop 0
	v_lshl_add_u64 v[44:45], v[44:45], 1, s[50:51]
	s_waitcnt vmcnt(9)
	s_nop 1
	v_pk_mov_b32 v[36:37], v[174:175], v[174:175] op_sel:[0,1]
	v_pk_mov_b32 v[38:39], v[176:177], v[176:177] op_sel:[0,1]
	v_pk_add_f32 v[38:39], v[32:33], v[38:39]
	v_pk_add_f32 v[36:37], v[30:31], v[36:37]
	s_nop 1
	v_pk_mov_b32 v[40:41], v[178:179], v[178:179] op_sel:[0,1]
	v_pk_mov_b32 v[42:43], v[180:181], v[180:181] op_sel:[0,1]
	v_pk_add_f32 v[42:43], v[28:29], v[42:43]
	v_pk_add_f32 v[40:41], v[26:27], v[40:41]
	v_cvt_pk_bf16_f32 v26, v36, v37
	v_cvt_pk_bf16_f32 v27, v38, v39
	v_mul_f32_e32 v37, v37, v37
	v_cvt_pk_bf16_f32 v28, v40, v41
	v_cvt_pk_bf16_f32 v29, v42, v43
	global_store_dwordx4 v[44:45], v[26:29], off
	s_nop 0
	s_nop 0
	s_nop 0
	v_mul_f32_e32 v39, v39, v39
	v_mul_f32_e32 v41, v41, v41
	v_mul_f32_e32 v43, v43, v43
	v_fmac_f32_e32 v37, v36, v36
	v_fmac_f32_e32 v39, v38, v38
	v_fmac_f32_e32 v41, v40, v40
	v_fmac_f32_e32 v43, v42, v42
	v_add_f32_e32 v36, v37, v39
	v_add_f32_e32 v37, v41, v43
	v_add_f32_e32 v36, v36, v37
	s_nop 1
	v_pk_mov_b32 v[26:27], v[182:183], v[182:183] op_sel:[0,1]
	v_pk_mov_b32 v[28:29], v[184:185], v[184:185] op_sel:[0,1]
	v_pk_add_f32 v[24:25], v[24:25], v[28:29]
	v_pk_add_f32 v[22:23], v[22:23], v[26:27]
	s_nop 1
	v_pk_mov_b32 v[30:31], v[190:191], v[190:191] op_sel:[0,1]
	v_pk_mov_b32 v[32:33], v[192:193], v[192:193] op_sel:[0,1]
	v_pk_add_f32 v[26:27], v[20:21], v[32:33]
	v_pk_add_f32 v[28:29], v[18:19], v[30:31]
	v_mul_f32_e32 v18, v23, v23
	v_mul_f32_e32 v19, v25, v25
	v_mul_f32_e32 v20, v29, v29
	v_mul_f32_e32 v21, v27, v27
	v_fmac_f32_e32 v18, v22, v22
	v_fmac_f32_e32 v19, v24, v24
	v_fmac_f32_e32 v20, v28, v28
	v_fmac_f32_e32 v21, v26, v26
	v_add_f32_e32 v18, v18, v19
	v_add_f32_e32 v19, v20, v21
	v_add_f32_e32 v18, v18, v19
	v_add_f32_e32 v18, v36, v18
	ds_bpermute_b32 v19, v122, v18
	v_cvt_pk_bf16_f32 v20, v22, v23
	v_cvt_pk_bf16_f32 v21, v24, v25
	v_cvt_pk_bf16_f32 v22, v28, v29
	v_cvt_pk_bf16_f32 v23, v26, v27
	s_waitcnt lgkmcnt(0)
	v_add_f32_e32 v18, v18, v19
	ds_bpermute_b32 v19, v116, v18
	global_store_dwordx4 v[44:45], v[20:23], off offset:256
	s_and_saveexec_b64 s[24:25], s[4:5]
	s_cbranch_execz .LBB0_401
	s_waitcnt lgkmcnt(0)
	v_add_f32_e32 v18, v18, v19
	v_fma_f32 v18, v18, s55, 0.5
	v_trunc_f32_e32 v18, v18
	v_mul_f32_e32 v19, 0x2f800000, v18
	v_floor_f32_e32 v19, v19
	v_fmac_f32_e32 v18, 0xcf800000, v19
	v_cvt_u32_f32_e32 v18, v18
	v_cvt_u32_f32_e32 v19, v19
	v_lshl_add_u64 v[20:21], v[34:35], 3, s[10:11]
	global_atomic_add_x2 v[20:21], v[18:19], off
.LBB0_401:
	s_or_b64 exec, exec, s[24:25]
	v_add_u32_e32 v18, 0xb0, v150
	s_waitcnt lgkmcnt(0)
	v_ashrrev_i32_e32 v19, 31, v18
	v_lshlrev_b64 v[20:21], 11, v[18:19]
	v_lshl_add_u64 v[28:29], v[20:21], 0, v[148:149]
	v_lshl_add_u64 v[30:31], v[28:29], 2, s[48:49]
	s_nop 0
	s_nop 0
	v_lshl_add_u64 v[28:29], v[28:29], 1, s[50:51]
	s_waitcnt vmcnt(5)
	s_nop 1
	v_pk_mov_b32 v[20:21], v[194:195], v[194:195] op_sel:[0,1]
	v_pk_mov_b32 v[22:23], v[196:197], v[196:197] op_sel:[0,1]
	v_pk_add_f32 v[22:23], v[16:17], v[22:23]
	v_pk_add_f32 v[20:21], v[14:15], v[20:21]
	s_nop 1
	v_pk_mov_b32 v[24:25], v[198:199], v[198:199] op_sel:[0,1]
	v_pk_mov_b32 v[26:27], v[200:201], v[200:201] op_sel:[0,1]
	v_pk_add_f32 v[26:27], v[12:13], v[26:27]
	v_pk_add_f32 v[24:25], v[10:11], v[24:25]
	v_cvt_pk_bf16_f32 v10, v20, v21
	v_cvt_pk_bf16_f32 v11, v22, v23
	v_mul_f32_e32 v21, v21, v21
	v_cvt_pk_bf16_f32 v12, v24, v25
	v_cvt_pk_bf16_f32 v13, v26, v27
	global_store_dwordx4 v[28:29], v[10:13], off
	s_nop 0
	s_nop 0
	s_nop 0
	v_mul_f32_e32 v23, v23, v23
	v_mul_f32_e32 v25, v25, v25
	v_mul_f32_e32 v27, v27, v27
	v_fmac_f32_e32 v21, v20, v20
	v_fmac_f32_e32 v23, v22, v22
	v_fmac_f32_e32 v25, v24, v24
	v_fmac_f32_e32 v27, v26, v26
	v_add_f32_e32 v20, v21, v23
	v_add_f32_e32 v21, v25, v27
	v_add_f32_e32 v20, v20, v21
	s_nop 1
	v_pk_mov_b32 v[10:11], v[202:203], v[202:203] op_sel:[0,1]
	v_pk_mov_b32 v[12:13], v[204:205], v[204:205] op_sel:[0,1]
	v_pk_add_f32 v[8:9], v[8:9], v[12:13]
	v_pk_add_f32 v[6:7], v[6:7], v[10:11]
	s_nop 1
	v_pk_mov_b32 v[14:15], v[206:207], v[206:207] op_sel:[0,1]
	v_pk_mov_b32 v[16:17], v[208:209], v[208:209] op_sel:[0,1]
	v_pk_add_f32 v[10:11], v[4:5], v[16:17]
	v_pk_add_f32 v[12:13], v[2:3], v[14:15]
	v_mul_f32_e32 v2, v7, v7
	v_mul_f32_e32 v3, v9, v9
	v_mul_f32_e32 v4, v13, v13
	v_mul_f32_e32 v5, v11, v11
	v_fmac_f32_e32 v2, v6, v6
	v_fmac_f32_e32 v3, v8, v8
	v_fmac_f32_e32 v4, v12, v12
	v_fmac_f32_e32 v5, v10, v10
	v_add_f32_e32 v2, v2, v3
	v_add_f32_e32 v3, v4, v5
	v_add_f32_e32 v2, v2, v3
	v_add_f32_e32 v2, v20, v2
	ds_bpermute_b32 v3, v122, v2
	v_cvt_pk_bf16_f32 v4, v6, v7
	v_cvt_pk_bf16_f32 v5, v8, v9
	v_cvt_pk_bf16_f32 v6, v12, v13
	v_cvt_pk_bf16_f32 v7, v10, v11
	s_waitcnt lgkmcnt(0)
	v_add_f32_e32 v2, v2, v3
	ds_bpermute_b32 v3, v116, v2
	global_store_dwordx4 v[28:29], v[4:7], off offset:256
	s_and_saveexec_b64 s[24:25], s[4:5]
	s_cbranch_execz .LBB0_403
	s_waitcnt lgkmcnt(0)
	v_add_f32_e32 v2, v2, v3
	v_fma_f32 v2, v2, s55, 0.5
	v_trunc_f32_e32 v2, v2
	v_mul_f32_e32 v3, 0x2f800000, v2
	v_floor_f32_e32 v3, v3
	v_fmac_f32_e32 v2, 0xcf800000, v3
	v_cvt_u32_f32_e32 v2, v2
	v_cvt_u32_f32_e32 v3, v3
	v_lshl_add_u64 v[4:5], v[18:19], 3, s[10:11]
	global_atomic_add_x2 v[4:5], v[2:3], off

.LBB0_470:
	s_ashr_i32 s19, s18, 31
	s_lshl_b64 s[20:21], s[18:19], 20
	s_add_u32 s20, s50, s20
	s_addc_u32 s21, s51, s21
	s_and_b64 s[22:23], s[4:5], exec
	s_cselect_b32 s19, s21, s27
	s_cselect_b32 s55, s20, s26
	s_ashr_i32 s17, s16, 31
	s_lshl_b64 s[22:23], s[16:17], 20
	s_add_u32 s22, s3, s22
	s_addc_u32 s23, s33, s23
	s_and_b64 s[30:31], s[4:5], exec
	s_cselect_b32 s17, s23, s29
	s_cselect_b32 s56, s22, s28
	s_add_u32 s26, s26, 0x80080
	s_addc_u32 s27, s27, 0
	s_add_u32 s57, s28, 0x100
	v_mov_b32_e32 v10, 0
	s_addc_u32 s58, s29, 0
	s_mov_b32 s59, -2
	v_mov_b32_e32 v11, v10
	v_pk_mov_b32 v[2:3], v[10:11], v[10:11]
	v_pk_mov_b32 v[4:5], v[10:11], v[10:11]
	v_pk_mov_b32 v[6:7], v[10:11], v[10:11]
	v_pk_mov_b32 v[8:9], v[10:11], v[10:11]
	v_pk_mov_b32 v[12:13], v[10:11], v[10:11]
	v_pk_mov_b32 v[14:15], v[10:11], v[10:11]
	v_pk_mov_b32 v[16:17], v[10:11], v[10:11]
	v_pk_mov_b32 v[18:19], v[10:11], v[10:11]
	v_pk_mov_b32 v[20:21], v[10:11], v[10:11]
	v_pk_mov_b32 v[22:23], v[10:11], v[10:11]
	v_pk_mov_b32 v[24:25], v[10:11], v[10:11]
	v_pk_mov_b32 v[26:27], v[10:11], v[10:11]
	v_pk_mov_b32 v[28:29], v[10:11], v[10:11]
	v_pk_mov_b32 v[30:31], v[10:11], v[10:11]
	v_pk_mov_b32 v[32:33], v[10:11], v[10:11]
	v_pk_mov_b32 v[34:35], v[10:11], v[10:11]
	v_pk_mov_b32 v[36:37], v[10:11], v[10:11]
	v_pk_mov_b32 v[38:39], v[10:11], v[10:11]
	v_pk_mov_b32 v[40:41], v[10:11], v[10:11]
	v_pk_mov_b32 v[42:43], v[10:11], v[10:11]
	v_pk_mov_b32 v[44:45], v[10:11], v[10:11]
	v_pk_mov_b32 v[46:47], v[10:11], v[10:11]
	v_pk_mov_b32 v[48:49], v[10:11], v[10:11]
	v_pk_mov_b32 v[50:51], v[10:11], v[10:11]
	v_pk_mov_b32 v[52:53], v[10:11], v[10:11]
	v_pk_mov_b32 v[54:55], v[10:11], v[10:11]
	v_pk_mov_b32 v[56:57], v[10:11], v[10:11]
	v_pk_mov_b32 v[58:59], v[10:11], v[10:11]
	v_pk_mov_b32 v[60:61], v[10:11], v[10:11]
	v_pk_mov_b32 v[62:63], v[10:11], v[10:11]
	v_pk_mov_b32 v[64:65], v[10:11], v[10:11]
	v_pk_mov_b32 v[66:67], v[10:11], v[10:11]
	v_pk_mov_b32 v[68:69], v[10:11], v[10:11]
	v_pk_mov_b32 v[70:71], v[10:11], v[10:11]
	v_pk_mov_b32 v[72:73], v[10:11], v[10:11]
	v_pk_mov_b32 v[74:75], v[10:11], v[10:11]
	v_pk_mov_b32 v[76:77], v[10:11], v[10:11]
	v_pk_mov_b32 v[78:79], v[10:11], v[10:11]
	v_pk_mov_b32 v[80:81], v[10:11], v[10:11]
	v_pk_mov_b32 v[82:83], v[10:11], v[10:11]
	v_pk_mov_b32 v[84:85], v[10:11], v[10:11]
	v_pk_mov_b32 v[86:87], v[10:11], v[10:11]
	v_pk_mov_b32 v[88:89], v[10:11], v[10:11]
	v_pk_mov_b32 v[90:91], v[10:11], v[10:11]
	v_pk_mov_b32 v[92:93], v[10:11], v[10:11]
	v_pk_mov_b32 v[94:95], v[10:11], v[10:11]
	v_pk_mov_b32 v[96:97], v[10:11], v[10:11]
	v_pk_mov_b32 v[98:99], v[10:11], v[10:11]
	v_pk_mov_b32 v[100:101], v[10:11], v[10:11]
	v_pk_mov_b32 v[102:103], v[10:11], v[10:11]
	v_pk_mov_b32 v[104:105], v[10:11], v[10:11]
	v_pk_mov_b32 v[106:107], v[10:11], v[10:11]
	v_pk_mov_b32 v[108:109], v[10:11], v[10:11]
	v_pk_mov_b32 v[110:111], v[10:11], v[10:11]
	v_pk_mov_b32 v[112:113], v[10:11], v[10:11]
	v_pk_mov_b32 v[114:115], v[10:11], v[10:11]
	v_pk_mov_b32 v[116:117], v[10:11], v[10:11]
	v_pk_mov_b32 v[118:119], v[10:11], v[10:11]
	v_pk_mov_b32 v[120:121], v[10:11], v[10:11]
	v_pk_mov_b32 v[122:123], v[10:11], v[10:11]
	v_pk_mov_b32 v[124:125], v[10:11], v[10:11]
	v_pk_mov_b32 v[126:127], v[10:11], v[10:11]
	v_pk_mov_b32 v[128:129], v[10:11], v[10:11]

.LBB0_555:
	s_add_u32 s20, s20, 0xb0080
	s_addc_u32 s21, s21, 0
	s_add_u32 s49, s22, 0x100
	v_mov_b32_e32 v2, 0
	s_addc_u32 s54, s23, 0
	s_mov_b32 s55, -2
	s_waitcnt lgkmcnt(0)
	v_mov_b32_e32 v3, v2
	v_pk_mov_b32 v[4:5], v[2:3], v[2:3]
	v_pk_mov_b32 v[6:7], v[2:3], v[2:3]
	v_pk_mov_b32 v[8:9], v[2:3], v[2:3]
	v_pk_mov_b32 v[10:11], v[2:3], v[2:3]
	v_pk_mov_b32 v[12:13], v[2:3], v[2:3]
	v_pk_mov_b32 v[14:15], v[2:3], v[2:3]
	v_pk_mov_b32 v[16:17], v[2:3], v[2:3]
	v_pk_mov_b32 v[18:19], v[2:3], v[2:3]
	v_pk_mov_b32 v[20:21], v[2:3], v[2:3]
	v_pk_mov_b32 v[22:23], v[2:3], v[2:3]
	v_pk_mov_b32 v[24:25], v[2:3], v[2:3]
	v_pk_mov_b32 v[26:27], v[2:3], v[2:3]
	v_pk_mov_b32 v[28:29], v[2:3], v[2:3]
	v_pk_mov_b32 v[30:31], v[2:3], v[2:3]
	v_pk_mov_b32 v[32:33], v[2:3], v[2:3]
	v_pk_mov_b32 v[34:35], v[2:3], v[2:3]
	v_pk_mov_b32 v[36:37], v[2:3], v[2:3]
	v_pk_mov_b32 v[38:39], v[2:3], v[2:3]
	v_pk_mov_b32 v[40:41], v[2:3], v[2:3]
	v_pk_mov_b32 v[42:43], v[2:3], v[2:3]
	v_pk_mov_b32 v[44:45], v[2:3], v[2:3]
	v_pk_mov_b32 v[46:47], v[2:3], v[2:3]
	v_pk_mov_b32 v[48:49], v[2:3], v[2:3]
	v_pk_mov_b32 v[50:51], v[2:3], v[2:3]
	v_pk_mov_b32 v[52:53], v[2:3], v[2:3]
	v_pk_mov_b32 v[54:55], v[2:3], v[2:3]
	v_pk_mov_b32 v[56:57], v[2:3], v[2:3]
	v_pk_mov_b32 v[58:59], v[2:3], v[2:3]
	v_pk_mov_b32 v[60:61], v[2:3], v[2:3]
	v_pk_mov_b32 v[62:63], v[2:3], v[2:3]
	v_pk_mov_b32 v[64:65], v[2:3], v[2:3]
	v_pk_mov_b32 v[66:67], v[2:3], v[2:3]
	v_pk_mov_b32 v[68:69], v[2:3], v[2:3]
	v_pk_mov_b32 v[70:71], v[2:3], v[2:3]
	v_pk_mov_b32 v[72:73], v[2:3], v[2:3]
	v_pk_mov_b32 v[74:75], v[2:3], v[2:3]
	v_pk_mov_b32 v[76:77], v[2:3], v[2:3]
	v_pk_mov_b32 v[78:79], v[2:3], v[2:3]
	v_pk_mov_b32 v[80:81], v[2:3], v[2:3]
	v_pk_mov_b32 v[82:83], v[2:3], v[2:3]
	v_pk_mov_b32 v[84:85], v[2:3], v[2:3]
	v_pk_mov_b32 v[86:87], v[2:3], v[2:3]
	v_pk_mov_b32 v[88:89], v[2:3], v[2:3]
	v_pk_mov_b32 v[90:91], v[2:3], v[2:3]
	v_pk_mov_b32 v[92:93], v[2:3], v[2:3]
	v_pk_mov_b32 v[94:95], v[2:3], v[2:3]
	v_pk_mov_b32 v[96:97], v[2:3], v[2:3]
	v_pk_mov_b32 v[98:99], v[2:3], v[2:3]
	v_pk_mov_b32 v[100:101], v[2:3], v[2:3]
	v_pk_mov_b32 v[102:103], v[2:3], v[2:3]
	v_pk_mov_b32 v[104:105], v[2:3], v[2:3]
	v_pk_mov_b32 v[106:107], v[2:3], v[2:3]
	v_pk_mov_b32 v[108:109], v[2:3], v[2:3]
	v_pk_mov_b32 v[110:111], v[2:3], v[2:3]
	v_pk_mov_b32 v[112:113], v[2:3], v[2:3]
	v_pk_mov_b32 v[114:115], v[2:3], v[2:3]
	v_pk_mov_b32 v[116:117], v[2:3], v[2:3]
	v_pk_mov_b32 v[118:119], v[2:3], v[2:3]
	v_pk_mov_b32 v[120:121], v[2:3], v[2:3]
	v_pk_mov_b32 v[122:123], v[2:3], v[2:3]
	v_pk_mov_b32 v[124:125], v[2:3], v[2:3]
	v_pk_mov_b32 v[126:127], v[2:3], v[2:3]
	v_pk_mov_b32 v[128:129], v[2:3], v[2:3]

.LBB0_559:
	v_lshl_add_u32 v150, s45, 8, v152
	v_ashrrev_i32_e32 v151, 31, v150
	v_lshl_or_b32 v148, s48, 8, v154
	v_lshlrev_b64 v[162:163], 12, v[150:151]
	v_ashrrev_i32_e32 v149, 31, v148
	v_lshl_add_u64 v[162:163], s[50:51], 0, v[162:163]
	v_lshl_add_u64 v[166:167], v[148:149], 1, v[162:163]
	v_mov_b32_e32 v184, v166
	v_mov_b32_e32 v185, v167
	v_mov_b32_e32 v222, 0x10000
	v_mov_b32_e32 v223, 0
	global_load_dwordx4 v[176:179], v[184:185], off
	global_load_dwordx4 v[180:183], v[184:185], off offset:256
	v_lshl_add_u64 v[184:185], v[222:223], 0, v[184:185]
	global_load_dwordx4 v[190:193], v[184:185], off
	global_load_dwordx4 v[194:197], v[184:185], off offset:256
	v_lshl_add_u64 v[184:185], v[222:223], 0, v[184:185]
	global_load_dwordx4 v[198:201], v[184:185], off
	global_load_dwordx4 v[202:205], v[184:185], off offset:256
	v_lshl_add_u64 v[184:185], v[222:223], 0, v[184:185]
	global_load_dwordx4 v[206:209], v[184:185], off
	global_load_dwordx4 v[210:213], v[184:185], off offset:256
	v_lshl_add_u64 v[184:185], v[222:223], 2, v[184:185]
	v_lshl_add_u64 v[184:185], v[222:223], 0, v[184:185]
	global_load_dwordx4 v[214:217], v[184:185], off
	global_load_dwordx4 v[218:221], v[184:185], off offset:256
	s_nop 0
	v_xor_b32_e32 v174, 32, v161
	s_waitcnt vmcnt(8)
	s_nop 1
	v_pk_mov_b32 v[162:163], v[176:177], v[176:177] op_sel:[0,1]
	v_pk_mov_b32 v[164:165], v[178:179], v[178:179] op_sel:[0,1]
	v_lshlrev_b32_e32 v168, 16, v162
	v_and_b32_e32 v169, 0xffff0000, v162
	v_lshlrev_b32_e32 v162, 16, v163
	v_and_b32_e32 v163, 0xffff0000, v163
	v_lshlrev_b32_e32 v170, 16, v164
	v_and_b32_e32 v171, 0xffff0000, v164
	v_lshlrev_b32_e32 v164, 16, v165
	v_and_b32_e32 v165, 0xffff0000, v165
	v_pk_add_f32 v[128:129], v[128:129], v[162:163]
	v_pk_add_f32 v[168:169], v[126:127], v[168:169]
	v_pk_add_f32 v[172:173], v[124:125], v[164:165]
	v_pk_add_f32 v[170:171], v[122:123], v[170:171]
	v_cvt_pk_bf16_f32 v124, v168, v169
	v_cvt_pk_bf16_f32 v125, v128, v129
	v_mul_f32_e32 v169, v169, v169
	v_cvt_pk_bf16_f32 v126, v170, v171
	v_cvt_pk_bf16_f32 v127, v172, v173
	s_nop 0
	v_mul_f32_e32 v129, v129, v129
	v_mul_f32_e32 v171, v171, v171
	v_mul_f32_e32 v173, v173, v173
	v_fmac_f32_e32 v169, v168, v168
	v_fmac_f32_e32 v129, v128, v128
	v_fmac_f32_e32 v171, v170, v170
	v_fmac_f32_e32 v173, v172, v172
	v_add_f32_e32 v128, v169, v129
	v_add_f32_e32 v129, v171, v173
	v_add_f32_e32 v170, v128, v129
	v_and_b32_e32 v123, 64, v161
	v_xor_b32_e32 v122, 16, v161
	v_add_u32_e32 v123, 64, v123
	v_cmp_lt_i32_e32 vcc, v122, v123
	global_store_dwordx4 v[166:167], v[124:127], off
	s_nop 1
	v_pk_mov_b32 v[162:163], v[180:181], v[180:181] op_sel:[0,1]
	v_pk_mov_b32 v[164:165], v[182:183], v[182:183] op_sel:[0,1]
	v_lshl_add_u64 v[184:185], v[222:223], 0, v[184:185]
	global_load_dwordx4 v[176:179], v[184:185], off
	global_load_dwordx4 v[180:183], v[184:185], off offset:256
	v_lshlrev_b32_e32 v128, 16, v162
	v_and_b32_e32 v129, 0xffff0000, v162
	v_lshlrev_b32_e32 v162, 16, v163
	v_and_b32_e32 v163, 0xffff0000, v163
	v_lshlrev_b32_e32 v168, 16, v164
	v_and_b32_e32 v169, 0xffff0000, v164
	v_lshlrev_b32_e32 v164, 16, v165
	v_and_b32_e32 v165, 0xffff0000, v165
	v_pk_add_f32 v[120:121], v[120:121], v[162:163]
	v_pk_add_f32 v[118:119], v[118:119], v[128:129]
	v_pk_add_f32 v[128:129], v[116:117], v[164:165]
	v_pk_add_f32 v[162:163], v[114:115], v[168:169]
	v_mul_f32_e32 v114, v119, v119
	v_mul_f32_e32 v115, v121, v121
	v_mul_f32_e32 v116, v163, v163
	v_mul_f32_e32 v117, v129, v129
	v_fmac_f32_e32 v114, v118, v118
	v_fmac_f32_e32 v115, v120, v120
	v_fmac_f32_e32 v116, v162, v162
	v_fmac_f32_e32 v117, v128, v128
	v_add_f32_e32 v114, v114, v115
	v_add_f32_e32 v115, v116, v117
	v_cndmask_b32_e32 v122, v161, v122, vcc
	v_add_f32_e32 v114, v114, v115
	v_lshlrev_b32_e32 v122, 2, v122
	v_add_f32_e32 v114, v170, v114
	ds_bpermute_b32 v115, v122, v114
	v_cmp_lt_i32_e32 vcc, v174, v123
	v_cvt_pk_bf16_f32 v118, v118, v119
	v_cvt_pk_bf16_f32 v119, v120, v121
	v_cvt_pk_bf16_f32 v120, v162, v163
	s_waitcnt lgkmcnt(0)
	v_add_f32_e32 v114, v114, v115
	v_cvt_pk_bf16_f32 v121, v128, v129
	v_cndmask_b32_e32 v116, v161, v174, vcc
	v_lshlrev_b32_e32 v116, 2, v116
	ds_bpermute_b32 v115, v116, v114
	global_store_dwordx4 v[166:167], v[118:121], off offset:256
	s_and_saveexec_b64 s[20:21], s[4:5]
	s_cbranch_execz .LBB0_561
	s_waitcnt lgkmcnt(0)
	v_add_f32_e32 v114, v114, v115
	v_fma_f32 v114, v114, s42, 0.5
	v_trunc_f32_e32 v114, v114
	v_mul_f32_e32 v115, 0x2f800000, v114
	v_floor_f32_e32 v115, v115
	v_fmac_f32_e32 v114, 0xcf800000, v115
	v_cvt_u32_f32_e32 v114, v114
	v_cvt_u32_f32_e32 v115, v115
	v_lshl_add_u64 v[118:119], v[150:151], 3, s[12:13]
	global_atomic_add_x2 v[118:119], v[114:115], off
.LBB0_561:
	s_or_b64 exec, exec, s[20:21]
	v_or_b32_e32 v114, 16, v150
	s_waitcnt lgkmcnt(0)
	v_ashrrev_i32_e32 v115, 31, v114
	v_lshlrev_b64 v[118:119], 12, v[114:115]
	v_lshl_add_u64 v[118:119], s[50:51], 0, v[118:119]
	v_lshl_add_u64 v[124:125], v[148:149], 1, v[118:119]
	s_nop 0
	s_waitcnt vmcnt(10)
	s_nop 1
	v_pk_mov_b32 v[118:119], v[190:191], v[190:191] op_sel:[0,1]
	v_pk_mov_b32 v[120:121], v[192:193], v[192:193] op_sel:[0,1]
	v_lshlrev_b32_e32 v126, 16, v118
	v_and_b32_e32 v127, 0xffff0000, v118
	v_lshlrev_b32_e32 v118, 16, v119
	v_and_b32_e32 v119, 0xffff0000, v119
	v_lshlrev_b32_e32 v128, 16, v120
	v_and_b32_e32 v129, 0xffff0000, v120
	v_lshlrev_b32_e32 v120, 16, v121
	v_and_b32_e32 v121, 0xffff0000, v121
	v_pk_add_f32 v[118:119], v[112:113], v[118:119]
	v_pk_add_f32 v[126:127], v[110:111], v[126:127]
	v_pk_add_f32 v[120:121], v[108:109], v[120:121]
	v_pk_add_f32 v[128:129], v[106:107], v[128:129]
	v_cvt_pk_bf16_f32 v106, v126, v127
	v_cvt_pk_bf16_f32 v107, v118, v119
	v_mul_f32_e32 v117, v127, v127
	v_cvt_pk_bf16_f32 v108, v128, v129
	v_cvt_pk_bf16_f32 v109, v120, v121
	s_nop 0
	v_mul_f32_e32 v119, v119, v119
	v_mul_f32_e32 v123, v129, v129
	v_mul_f32_e32 v121, v121, v121
	v_fmac_f32_e32 v117, v126, v126
	v_fmac_f32_e32 v119, v118, v118
	v_fmac_f32_e32 v123, v128, v128
	v_fmac_f32_e32 v121, v120, v120
	v_add_f32_e32 v117, v117, v119
	v_add_f32_e32 v118, v123, v121
	v_add_f32_e32 v117, v117, v118
	global_store_dwordx4 v[124:125], v[106:109], off
	s_nop 1
	v_pk_mov_b32 v[110:111], v[194:195], v[194:195] op_sel:[0,1]
	v_pk_mov_b32 v[112:113], v[196:197], v[196:197] op_sel:[0,1]
	v_lshl_add_u64 v[184:185], v[222:223], 0, v[184:185]
	global_load_dwordx4 v[190:193], v[184:185], off
	global_load_dwordx4 v[194:197], v[184:185], off offset:256
	v_lshlrev_b32_e32 v118, 16, v110
	v_and_b32_e32 v119, 0xffff0000, v110
	v_lshlrev_b32_e32 v110, 16, v111
	v_and_b32_e32 v111, 0xffff0000, v111
	v_lshlrev_b32_e32 v120, 16, v112
	v_and_b32_e32 v121, 0xffff0000, v112
	v_lshlrev_b32_e32 v112, 16, v113
	v_and_b32_e32 v113, 0xffff0000, v113
	v_pk_add_f32 v[104:105], v[104:105], v[110:111]
	v_pk_add_f32 v[102:103], v[102:103], v[118:119]
	v_pk_add_f32 v[110:111], v[100:101], v[112:113]
	v_pk_add_f32 v[112:113], v[98:99], v[120:121]
	v_mul_f32_e32 v98, v103, v103
	v_mul_f32_e32 v99, v105, v105
	v_mul_f32_e32 v100, v113, v113
	v_mul_f32_e32 v101, v111, v111
	v_fmac_f32_e32 v98, v102, v102
	v_fmac_f32_e32 v99, v104, v104
	v_fmac_f32_e32 v100, v112, v112
	v_fmac_f32_e32 v101, v110, v110
	v_add_f32_e32 v98, v98, v99
	v_add_f32_e32 v99, v100, v101
	v_add_f32_e32 v98, v98, v99
	v_add_f32_e32 v98, v117, v98
	ds_bpermute_b32 v99, v122, v98
	v_cvt_pk_bf16_f32 v100, v102, v103
	v_cvt_pk_bf16_f32 v101, v104, v105
	v_cvt_pk_bf16_f32 v102, v112, v113
	v_cvt_pk_bf16_f32 v103, v110, v111
	s_waitcnt lgkmcnt(0)
	v_add_f32_e32 v98, v98, v99
	ds_bpermute_b32 v99, v116, v98
	global_store_dwordx4 v[124:125], v[100:103], off offset:256
	s_and_saveexec_b64 s[20:21], s[4:5]
	s_cbranch_execz .LBB0_563
	s_waitcnt lgkmcnt(0)
	v_add_f32_e32 v98, v98, v99
	v_fma_f32 v98, v98, s42, 0.5
	v_trunc_f32_e32 v98, v98
	v_mul_f32_e32 v99, 0x2f800000, v98
	v_floor_f32_e32 v99, v99
	v_fmac_f32_e32 v98, 0xcf800000, v99
	v_cvt_u32_f32_e32 v98, v98
	v_cvt_u32_f32_e32 v99, v99
	v_lshl_add_u64 v[100:101], v[114:115], 3, s[12:13]
	global_atomic_add_x2 v[100:101], v[98:99], off
.LBB0_563:
	s_or_b64 exec, exec, s[20:21]
	v_or_b32_e32 v98, 32, v150
	s_waitcnt lgkmcnt(0)
	v_ashrrev_i32_e32 v99, 31, v98
	v_lshlrev_b64 v[100:101], 12, v[98:99]
	v_lshl_add_u64 v[100:101], s[50:51], 0, v[100:101]
	v_lshl_add_u64 v[104:105], v[148:149], 1, v[100:101]
	s_nop 0
	s_waitcnt vmcnt(12)
	s_nop 1
	v_pk_mov_b32 v[100:101], v[198:199], v[198:199] op_sel:[0,1]
	v_pk_mov_b32 v[102:103], v[200:201], v[200:201] op_sel:[0,1]
	v_lshlrev_b32_e32 v106, 16, v100
	v_and_b32_e32 v107, 0xffff0000, v100
	v_lshlrev_b32_e32 v100, 16, v101
	v_and_b32_e32 v101, 0xffff0000, v101
	v_lshlrev_b32_e32 v108, 16, v102
	v_and_b32_e32 v109, 0xffff0000, v102
	v_lshlrev_b32_e32 v102, 16, v103
	v_and_b32_e32 v103, 0xffff0000, v103
	v_pk_add_f32 v[100:101], v[96:97], v[100:101]
	v_pk_add_f32 v[106:107], v[94:95], v[106:107]
	v_pk_add_f32 v[102:103], v[92:93], v[102:103]
	v_pk_add_f32 v[108:109], v[90:91], v[108:109]
	v_cvt_pk_bf16_f32 v90, v106, v107
	v_cvt_pk_bf16_f32 v91, v100, v101
	v_mul_f32_e32 v107, v107, v107
	v_cvt_pk_bf16_f32 v92, v108, v109
	v_cvt_pk_bf16_f32 v93, v102, v103
	s_nop 0
	v_mul_f32_e32 v101, v101, v101
	v_mul_f32_e32 v109, v109, v109
	v_mul_f32_e32 v103, v103, v103
	v_fmac_f32_e32 v107, v106, v106
	v_fmac_f32_e32 v101, v100, v100
	v_fmac_f32_e32 v109, v108, v108
	v_fmac_f32_e32 v103, v102, v102
	v_add_f32_e32 v100, v107, v101
	v_add_f32_e32 v101, v109, v103
	v_add_f32_e32 v106, v100, v101
	global_store_dwordx4 v[104:105], v[90:93], off
	s_nop 1
	v_pk_mov_b32 v[94:95], v[202:203], v[202:203] op_sel:[0,1]
	v_pk_mov_b32 v[96:97], v[204:205], v[204:205] op_sel:[0,1]
	v_lshl_add_u64 v[184:185], v[222:223], 0, v[184:185]
	global_load_dwordx4 v[198:201], v[184:185], off
	global_load_dwordx4 v[202:205], v[184:185], off offset:256
	v_lshlrev_b32_e32 v100, 16, v94
	v_and_b32_e32 v101, 0xffff0000, v94
	v_lshlrev_b32_e32 v94, 16, v95
	v_and_b32_e32 v95, 0xffff0000, v95
	v_lshlrev_b32_e32 v102, 16, v96
	v_and_b32_e32 v103, 0xffff0000, v96
	v_lshlrev_b32_e32 v96, 16, v97
	v_and_b32_e32 v97, 0xffff0000, v97
	v_pk_add_f32 v[88:89], v[88:89], v[94:95]
	v_pk_add_f32 v[86:87], v[86:87], v[100:101]
	v_pk_add_f32 v[94:95], v[84:85], v[96:97]
	v_pk_add_f32 v[96:97], v[82:83], v[102:103]
	v_mul_f32_e32 v82, v87, v87
	v_mul_f32_e32 v83, v89, v89
	v_mul_f32_e32 v84, v97, v97
	v_mul_f32_e32 v85, v95, v95
	v_fmac_f32_e32 v82, v86, v86
	v_fmac_f32_e32 v83, v88, v88
	v_fmac_f32_e32 v84, v96, v96
	v_fmac_f32_e32 v85, v94, v94
	v_add_f32_e32 v82, v82, v83
	v_add_f32_e32 v83, v84, v85
	v_add_f32_e32 v82, v82, v83
	v_add_f32_e32 v82, v106, v82
	ds_bpermute_b32 v83, v122, v82
	v_cvt_pk_bf16_f32 v84, v86, v87
	v_cvt_pk_bf16_f32 v85, v88, v89
	v_cvt_pk_bf16_f32 v86, v96, v97
	v_cvt_pk_bf16_f32 v87, v94, v95
	s_waitcnt lgkmcnt(0)
	v_add_f32_e32 v82, v82, v83
	ds_bpermute_b32 v83, v116, v82
	global_store_dwordx4 v[104:105], v[84:87], off offset:256
	s_and_saveexec_b64 s[20:21], s[4:5]
	s_cbranch_execz .LBB0_565
	s_waitcnt lgkmcnt(0)
	v_add_f32_e32 v82, v82, v83
	v_fma_f32 v82, v82, s42, 0.5
	v_trunc_f32_e32 v82, v82
	v_mul_f32_e32 v83, 0x2f800000, v82
	v_floor_f32_e32 v83, v83
	v_fmac_f32_e32 v82, 0xcf800000, v83
	v_cvt_u32_f32_e32 v82, v82
	v_cvt_u32_f32_e32 v83, v83
	v_lshl_add_u64 v[84:85], v[98:99], 3, s[12:13]
	global_atomic_add_x2 v[84:85], v[82:83], off
.LBB0_565:
	s_or_b64 exec, exec, s[20:21]
	v_or_b32_e32 v82, 48, v150
	s_waitcnt lgkmcnt(0)
	v_ashrrev_i32_e32 v83, 31, v82
	v_lshlrev_b64 v[84:85], 12, v[82:83]
	v_lshl_add_u64 v[84:85], s[50:51], 0, v[84:85]
	v_lshl_add_u64 v[88:89], v[148:149], 1, v[84:85]
	s_nop 0
	s_waitcnt vmcnt(14)
	s_nop 1
	v_pk_mov_b32 v[84:85], v[206:207], v[206:207] op_sel:[0,1]
	v_pk_mov_b32 v[86:87], v[208:209], v[208:209] op_sel:[0,1]
	v_lshlrev_b32_e32 v90, 16, v84
	v_and_b32_e32 v91, 0xffff0000, v84
	v_lshlrev_b32_e32 v84, 16, v85
	v_and_b32_e32 v85, 0xffff0000, v85
	v_lshlrev_b32_e32 v92, 16, v86
	v_and_b32_e32 v93, 0xffff0000, v86
	v_lshlrev_b32_e32 v86, 16, v87
	v_and_b32_e32 v87, 0xffff0000, v87
	v_pk_add_f32 v[84:85], v[80:81], v[84:85]
	v_pk_add_f32 v[90:91], v[78:79], v[90:91]
	v_pk_add_f32 v[86:87], v[76:77], v[86:87]
	v_pk_add_f32 v[92:93], v[74:75], v[92:93]
	v_cvt_pk_bf16_f32 v74, v90, v91
	v_cvt_pk_bf16_f32 v75, v84, v85
	v_mul_f32_e32 v91, v91, v91
	v_cvt_pk_bf16_f32 v76, v92, v93
	v_cvt_pk_bf16_f32 v77, v86, v87
	s_nop 0
	v_mul_f32_e32 v85, v85, v85
	v_mul_f32_e32 v93, v93, v93
	v_mul_f32_e32 v87, v87, v87
	v_fmac_f32_e32 v91, v90, v90
	v_fmac_f32_e32 v85, v84, v84
	v_fmac_f32_e32 v93, v92, v92
	v_fmac_f32_e32 v87, v86, v86
	v_add_f32_e32 v84, v91, v85
	v_add_f32_e32 v85, v93, v87
	v_add_f32_e32 v90, v84, v85
	global_store_dwordx4 v[88:89], v[74:77], off
	s_nop 1
	v_pk_mov_b32 v[78:79], v[210:211], v[210:211] op_sel:[0,1]
	v_pk_mov_b32 v[80:81], v[212:213], v[212:213] op_sel:[0,1]
	v_lshlrev_b32_e32 v84, 16, v78
	v_and_b32_e32 v85, 0xffff0000, v78
	v_lshlrev_b32_e32 v78, 16, v79
	v_and_b32_e32 v79, 0xffff0000, v79
	v_lshlrev_b32_e32 v86, 16, v80
	v_and_b32_e32 v87, 0xffff0000, v80
	v_lshlrev_b32_e32 v80, 16, v81
	v_and_b32_e32 v81, 0xffff0000, v81
	v_pk_add_f32 v[72:73], v[72:73], v[78:79]
	v_pk_add_f32 v[70:71], v[70:71], v[84:85]
	v_pk_add_f32 v[78:79], v[68:69], v[80:81]
	v_pk_add_f32 v[80:81], v[66:67], v[86:87]
	v_mul_f32_e32 v66, v71, v71
	v_mul_f32_e32 v67, v73, v73
	v_mul_f32_e32 v68, v81, v81
	v_mul_f32_e32 v69, v79, v79
	v_fmac_f32_e32 v66, v70, v70
	v_fmac_f32_e32 v67, v72, v72
	v_fmac_f32_e32 v68, v80, v80
	v_fmac_f32_e32 v69, v78, v78
	v_add_f32_e32 v66, v66, v67
	v_add_f32_e32 v67, v68, v69
	v_add_f32_e32 v66, v66, v67
	v_add_f32_e32 v66, v90, v66
	ds_bpermute_b32 v67, v122, v66
	v_cvt_pk_bf16_f32 v68, v70, v71
	v_cvt_pk_bf16_f32 v69, v72, v73
	v_cvt_pk_bf16_f32 v70, v80, v81
	v_cvt_pk_bf16_f32 v71, v78, v79
	s_waitcnt lgkmcnt(0)
	v_add_f32_e32 v66, v66, v67
	ds_bpermute_b32 v67, v116, v66
	global_store_dwordx4 v[88:89], v[68:71], off offset:256
	s_and_saveexec_b64 s[20:21], s[4:5]
	s_cbranch_execz .LBB0_567
	s_waitcnt lgkmcnt(0)
	v_add_f32_e32 v66, v66, v67
	v_fma_f32 v66, v66, s42, 0.5
	v_trunc_f32_e32 v66, v66
	v_mul_f32_e32 v67, 0x2f800000, v66
	v_floor_f32_e32 v67, v67
	v_fmac_f32_e32 v66, 0xcf800000, v67
	v_cvt_u32_f32_e32 v66, v66
	v_cvt_u32_f32_e32 v67, v67
	v_lshl_add_u64 v[68:69], v[82:83], 3, s[12:13]
	global_atomic_add_x2 v[68:69], v[66:67], off
.LBB0_567:
	s_or_b64 exec, exec, s[20:21]
	v_add_u32_e32 v66, 0x80, v150
	s_waitcnt lgkmcnt(0)
	v_ashrrev_i32_e32 v67, 31, v66
	v_lshlrev_b64 v[68:69], 12, v[66:67]
	v_lshl_add_u64 v[68:69], s[50:51], 0, v[68:69]
	v_lshl_add_u64 v[72:73], v[148:149], 1, v[68:69]
	s_nop 0
	s_waitcnt vmcnt(14)
	s_nop 1
	v_pk_mov_b32 v[68:69], v[214:215], v[214:215] op_sel:[0,1]
	v_pk_mov_b32 v[70:71], v[216:217], v[216:217] op_sel:[0,1]
	v_lshlrev_b32_e32 v74, 16, v68
	v_and_b32_e32 v75, 0xffff0000, v68
	v_lshlrev_b32_e32 v68, 16, v69
	v_and_b32_e32 v69, 0xffff0000, v69
	v_lshlrev_b32_e32 v76, 16, v70
	v_and_b32_e32 v77, 0xffff0000, v70
	v_lshlrev_b32_e32 v70, 16, v71
	v_and_b32_e32 v71, 0xffff0000, v71
	v_pk_add_f32 v[68:69], v[64:65], v[68:69]
	v_pk_add_f32 v[74:75], v[62:63], v[74:75]
	v_pk_add_f32 v[70:71], v[60:61], v[70:71]
	v_pk_add_f32 v[76:77], v[58:59], v[76:77]
	v_cvt_pk_bf16_f32 v58, v74, v75
	v_cvt_pk_bf16_f32 v59, v68, v69
	v_mul_f32_e32 v75, v75, v75
	v_cvt_pk_bf16_f32 v60, v76, v77
	v_cvt_pk_bf16_f32 v61, v70, v71
	s_nop 0
	v_mul_f32_e32 v69, v69, v69
	v_mul_f32_e32 v77, v77, v77
	v_mul_f32_e32 v71, v71, v71
	v_fmac_f32_e32 v75, v74, v74
	v_fmac_f32_e32 v69, v68, v68
	v_fmac_f32_e32 v77, v76, v76
	v_fmac_f32_e32 v71, v70, v70
	v_add_f32_e32 v68, v75, v69
	v_add_f32_e32 v69, v77, v71
	v_add_f32_e32 v74, v68, v69
	global_store_dwordx4 v[72:73], v[58:61], off
	s_nop 1
	v_pk_mov_b32 v[62:63], v[218:219], v[218:219] op_sel:[0,1]
	v_pk_mov_b32 v[64:65], v[220:221], v[220:221] op_sel:[0,1]
	v_lshlrev_b32_e32 v68, 16, v62
	v_and_b32_e32 v69, 0xffff0000, v62
	v_lshlrev_b32_e32 v62, 16, v63
	v_and_b32_e32 v63, 0xffff0000, v63
	v_lshlrev_b32_e32 v70, 16, v64
	v_and_b32_e32 v71, 0xffff0000, v64
	v_lshlrev_b32_e32 v64, 16, v65
	v_and_b32_e32 v65, 0xffff0000, v65
	v_pk_add_f32 v[56:57], v[56:57], v[62:63]
	v_pk_add_f32 v[54:55], v[54:55], v[68:69]
	v_pk_add_f32 v[62:63], v[52:53], v[64:65]
	v_pk_add_f32 v[64:65], v[50:51], v[70:71]
	v_mul_f32_e32 v50, v55, v55
	v_mul_f32_e32 v51, v57, v57
	v_mul_f32_e32 v52, v65, v65
	v_mul_f32_e32 v53, v63, v63
	v_fmac_f32_e32 v50, v54, v54
	v_fmac_f32_e32 v51, v56, v56
	v_fmac_f32_e32 v52, v64, v64
	v_fmac_f32_e32 v53, v62, v62
	v_add_f32_e32 v50, v50, v51
	v_add_f32_e32 v51, v52, v53
	v_add_f32_e32 v50, v50, v51
	v_add_f32_e32 v50, v74, v50
	ds_bpermute_b32 v51, v122, v50
	v_cvt_pk_bf16_f32 v52, v54, v55
	v_cvt_pk_bf16_f32 v53, v56, v57
	v_cvt_pk_bf16_f32 v54, v64, v65
	v_cvt_pk_bf16_f32 v55, v62, v63
	s_waitcnt lgkmcnt(0)
	v_add_f32_e32 v50, v50, v51
	ds_bpermute_b32 v51, v116, v50
	global_store_dwordx4 v[72:73], v[52:55], off offset:256
	s_and_saveexec_b64 s[20:21], s[4:5]
	s_cbranch_execz .LBB0_569
	s_waitcnt lgkmcnt(0)
	v_add_f32_e32 v50, v50, v51
	v_fma_f32 v50, v50, s42, 0.5
	v_trunc_f32_e32 v50, v50
	v_mul_f32_e32 v51, 0x2f800000, v50
	v_floor_f32_e32 v51, v51
	v_fmac_f32_e32 v50, 0xcf800000, v51
	v_cvt_u32_f32_e32 v50, v50
	v_cvt_u32_f32_e32 v51, v51
	v_lshl_add_u64 v[52:53], v[66:67], 3, s[12:13]
	global_atomic_add_x2 v[52:53], v[50:51], off
.LBB0_569:
	s_or_b64 exec, exec, s[20:21]
	v_add_u32_e32 v50, 0x90, v150
	s_waitcnt lgkmcnt(0)
	v_ashrrev_i32_e32 v51, 31, v50
	v_lshlrev_b64 v[52:53], 12, v[50:51]
	v_lshl_add_u64 v[52:53], s[50:51], 0, v[52:53]
	v_lshl_add_u64 v[56:57], v[148:149], 1, v[52:53]
	s_nop 0
	s_waitcnt vmcnt(13)
	s_nop 1
	v_pk_mov_b32 v[52:53], v[176:177], v[176:177] op_sel:[0,1]
	v_pk_mov_b32 v[54:55], v[178:179], v[178:179] op_sel:[0,1]
	v_lshlrev_b32_e32 v58, 16, v52
	v_and_b32_e32 v59, 0xffff0000, v52
	v_lshlrev_b32_e32 v52, 16, v53
	v_and_b32_e32 v53, 0xffff0000, v53
	v_lshlrev_b32_e32 v60, 16, v54
	v_and_b32_e32 v61, 0xffff0000, v54
	v_lshlrev_b32_e32 v54, 16, v55
	v_and_b32_e32 v55, 0xffff0000, v55
	v_pk_add_f32 v[52:53], v[48:49], v[52:53]
	v_pk_add_f32 v[58:59], v[46:47], v[58:59]
	v_pk_add_f32 v[54:55], v[44:45], v[54:55]
	v_pk_add_f32 v[60:61], v[42:43], v[60:61]
	v_cvt_pk_bf16_f32 v42, v58, v59
	v_cvt_pk_bf16_f32 v43, v52, v53
	v_mul_f32_e32 v59, v59, v59
	v_cvt_pk_bf16_f32 v44, v60, v61
	v_cvt_pk_bf16_f32 v45, v54, v55
	s_nop 0
	v_mul_f32_e32 v53, v53, v53
	v_mul_f32_e32 v61, v61, v61
	v_mul_f32_e32 v55, v55, v55
	v_fmac_f32_e32 v59, v58, v58
	v_fmac_f32_e32 v53, v52, v52
	v_fmac_f32_e32 v61, v60, v60
	v_fmac_f32_e32 v55, v54, v54
	v_add_f32_e32 v52, v59, v53
	v_add_f32_e32 v53, v61, v55
	v_add_f32_e32 v58, v52, v53
	global_store_dwordx4 v[56:57], v[42:45], off
	s_nop 1
	v_pk_mov_b32 v[46:47], v[180:181], v[180:181] op_sel:[0,1]
	v_pk_mov_b32 v[48:49], v[182:183], v[182:183] op_sel:[0,1]
	v_lshlrev_b32_e32 v52, 16, v46
	v_and_b32_e32 v53, 0xffff0000, v46
	v_lshlrev_b32_e32 v46, 16, v47
	v_and_b32_e32 v47, 0xffff0000, v47
	v_lshlrev_b32_e32 v54, 16, v48
	v_and_b32_e32 v55, 0xffff0000, v48
	v_lshlrev_b32_e32 v48, 16, v49
	v_and_b32_e32 v49, 0xffff0000, v49
	v_pk_add_f32 v[40:41], v[40:41], v[46:47]
	v_pk_add_f32 v[38:39], v[38:39], v[52:53]
	v_pk_add_f32 v[46:47], v[36:37], v[48:49]
	v_pk_add_f32 v[48:49], v[34:35], v[54:55]
	v_mul_f32_e32 v34, v39, v39
	v_mul_f32_e32 v35, v41, v41
	v_mul_f32_e32 v36, v49, v49
	v_mul_f32_e32 v37, v47, v47
	v_fmac_f32_e32 v34, v38, v38
	v_fmac_f32_e32 v35, v40, v40
	v_fmac_f32_e32 v36, v48, v48
	v_fmac_f32_e32 v37, v46, v46
	v_add_f32_e32 v34, v34, v35
	v_add_f32_e32 v35, v36, v37
	v_add_f32_e32 v34, v34, v35
	v_add_f32_e32 v34, v58, v34
	ds_bpermute_b32 v35, v122, v34
	v_cvt_pk_bf16_f32 v36, v38, v39
	v_cvt_pk_bf16_f32 v37, v40, v41
	v_cvt_pk_bf16_f32 v38, v48, v49
	v_cvt_pk_bf16_f32 v39, v46, v47
	s_waitcnt lgkmcnt(0)
	v_add_f32_e32 v34, v34, v35
	ds_bpermute_b32 v35, v116, v34
	global_store_dwordx4 v[56:57], v[36:39], off offset:256
	s_and_saveexec_b64 s[20:21], s[4:5]
	s_cbranch_execz .LBB0_571
	s_waitcnt lgkmcnt(0)
	v_add_f32_e32 v34, v34, v35
	v_fma_f32 v34, v34, s42, 0.5
	v_trunc_f32_e32 v34, v34
	v_mul_f32_e32 v35, 0x2f800000, v34
	v_floor_f32_e32 v35, v35
	v_fmac_f32_e32 v34, 0xcf800000, v35
	v_cvt_u32_f32_e32 v34, v34
	v_cvt_u32_f32_e32 v35, v35
	v_lshl_add_u64 v[36:37], v[50:51], 3, s[12:13]
	global_atomic_add_x2 v[36:37], v[34:35], off
.LBB0_571:
	s_or_b64 exec, exec, s[20:21]
	v_add_u32_e32 v34, 0xa0, v150
	s_waitcnt lgkmcnt(0)
	v_ashrrev_i32_e32 v35, 31, v34
	v_lshlrev_b64 v[36:37], 12, v[34:35]
	v_lshl_add_u64 v[36:37], s[50:51], 0, v[36:37]
	v_lshl_add_u64 v[40:41], v[148:149], 1, v[36:37]
	s_nop 0
	s_waitcnt vmcnt(11)
	s_nop 1
	v_pk_mov_b32 v[36:37], v[190:191], v[190:191] op_sel:[0,1]
	v_pk_mov_b32 v[38:39], v[192:193], v[192:193] op_sel:[0,1]
	v_lshlrev_b32_e32 v42, 16, v36
	v_and_b32_e32 v43, 0xffff0000, v36
	v_lshlrev_b32_e32 v36, 16, v37
	v_and_b32_e32 v37, 0xffff0000, v37
	v_lshlrev_b32_e32 v44, 16, v38
	v_and_b32_e32 v45, 0xffff0000, v38
	v_lshlrev_b32_e32 v38, 16, v39
	v_and_b32_e32 v39, 0xffff0000, v39
	v_pk_add_f32 v[36:37], v[32:33], v[36:37]
	v_pk_add_f32 v[42:43], v[30:31], v[42:43]
	v_pk_add_f32 v[38:39], v[28:29], v[38:39]
	v_pk_add_f32 v[44:45], v[26:27], v[44:45]
	v_cvt_pk_bf16_f32 v26, v42, v43
	v_cvt_pk_bf16_f32 v27, v36, v37
	v_mul_f32_e32 v43, v43, v43
	v_cvt_pk_bf16_f32 v28, v44, v45
	v_cvt_pk_bf16_f32 v29, v38, v39
	s_nop 0
	v_mul_f32_e32 v37, v37, v37
	v_mul_f32_e32 v45, v45, v45
	v_mul_f32_e32 v39, v39, v39
	v_fmac_f32_e32 v43, v42, v42
	v_fmac_f32_e32 v37, v36, v36
	v_fmac_f32_e32 v45, v44, v44
	v_fmac_f32_e32 v39, v38, v38
	v_add_f32_e32 v36, v43, v37
	v_add_f32_e32 v37, v45, v39
	v_add_f32_e32 v42, v36, v37
	global_store_dwordx4 v[40:41], v[26:29], off
	s_nop 1
	v_pk_mov_b32 v[30:31], v[194:195], v[194:195] op_sel:[0,1]
	v_pk_mov_b32 v[32:33], v[196:197], v[196:197] op_sel:[0,1]
	v_lshlrev_b32_e32 v36, 16, v30
	v_and_b32_e32 v37, 0xffff0000, v30
	v_lshlrev_b32_e32 v30, 16, v31
	v_and_b32_e32 v31, 0xffff0000, v31
	v_lshlrev_b32_e32 v38, 16, v32
	v_and_b32_e32 v39, 0xffff0000, v32
	v_lshlrev_b32_e32 v32, 16, v33
	v_and_b32_e32 v33, 0xffff0000, v33
	v_pk_add_f32 v[24:25], v[24:25], v[30:31]
	v_pk_add_f32 v[22:23], v[22:23], v[36:37]
	v_pk_add_f32 v[30:31], v[20:21], v[32:33]
	v_pk_add_f32 v[32:33], v[18:19], v[38:39]
	v_mul_f32_e32 v18, v23, v23
	v_mul_f32_e32 v19, v25, v25
	v_mul_f32_e32 v20, v33, v33
	v_mul_f32_e32 v21, v31, v31
	v_fmac_f32_e32 v18, v22, v22
	v_fmac_f32_e32 v19, v24, v24
	v_fmac_f32_e32 v20, v32, v32
	v_fmac_f32_e32 v21, v30, v30
	v_add_f32_e32 v18, v18, v19
	v_add_f32_e32 v19, v20, v21
	v_add_f32_e32 v18, v18, v19
	v_add_f32_e32 v18, v42, v18
	ds_bpermute_b32 v19, v122, v18
	v_cvt_pk_bf16_f32 v20, v22, v23
	v_cvt_pk_bf16_f32 v21, v24, v25
	v_cvt_pk_bf16_f32 v22, v32, v33
	v_cvt_pk_bf16_f32 v23, v30, v31
	s_waitcnt lgkmcnt(0)
	v_add_f32_e32 v18, v18, v19
	ds_bpermute_b32 v19, v116, v18
	global_store_dwordx4 v[40:41], v[20:23], off offset:256
	s_and_saveexec_b64 s[20:21], s[4:5]
	s_cbranch_execz .LBB0_573
	s_waitcnt lgkmcnt(0)
	v_add_f32_e32 v18, v18, v19
	v_fma_f32 v18, v18, s42, 0.5
	v_trunc_f32_e32 v18, v18
	v_mul_f32_e32 v19, 0x2f800000, v18
	v_floor_f32_e32 v19, v19
	v_fmac_f32_e32 v18, 0xcf800000, v19
	v_cvt_u32_f32_e32 v18, v18
	v_cvt_u32_f32_e32 v19, v19
	v_lshl_add_u64 v[20:21], v[34:35], 3, s[12:13]
	global_atomic_add_x2 v[20:21], v[18:19], off
.LBB0_573:
	s_or_b64 exec, exec, s[20:21]
	v_add_u32_e32 v18, 0xb0, v150
	s_waitcnt lgkmcnt(0)
	v_ashrrev_i32_e32 v19, 31, v18
	v_lshlrev_b64 v[20:21], 12, v[18:19]
	v_lshl_add_u64 v[20:21], s[50:51], 0, v[20:21]
	v_lshl_add_u64 v[24:25], v[148:149], 1, v[20:21]
	s_nop 0
	s_waitcnt vmcnt(9)
	s_nop 1
	v_pk_mov_b32 v[20:21], v[198:199], v[198:199] op_sel:[0,1]
	v_pk_mov_b32 v[22:23], v[200:201], v[200:201] op_sel:[0,1]
	v_lshlrev_b32_e32 v26, 16, v20
	v_and_b32_e32 v27, 0xffff0000, v20
	v_lshlrev_b32_e32 v20, 16, v21
	v_and_b32_e32 v21, 0xffff0000, v21
	v_lshlrev_b32_e32 v28, 16, v22
	v_and_b32_e32 v29, 0xffff0000, v22
	v_lshlrev_b32_e32 v22, 16, v23
	v_and_b32_e32 v23, 0xffff0000, v23
	v_pk_add_f32 v[20:21], v[16:17], v[20:21]
	v_pk_add_f32 v[26:27], v[14:15], v[26:27]
	v_pk_add_f32 v[22:23], v[12:13], v[22:23]
	v_pk_add_f32 v[28:29], v[10:11], v[28:29]
	v_cvt_pk_bf16_f32 v10, v26, v27
	v_cvt_pk_bf16_f32 v11, v20, v21
	v_mul_f32_e32 v27, v27, v27
	v_cvt_pk_bf16_f32 v12, v28, v29
	v_cvt_pk_bf16_f32 v13, v22, v23
	s_nop 0
	v_mul_f32_e32 v21, v21, v21
	v_mul_f32_e32 v29, v29, v29
	v_mul_f32_e32 v23, v23, v23
	v_fmac_f32_e32 v27, v26, v26
	v_fmac_f32_e32 v21, v20, v20
	v_fmac_f32_e32 v29, v28, v28
	v_fmac_f32_e32 v23, v22, v22
	v_add_f32_e32 v20, v27, v21
	v_add_f32_e32 v21, v29, v23
	v_add_f32_e32 v26, v20, v21
	global_store_dwordx4 v[24:25], v[10:13], off
	s_nop 1
	v_pk_mov_b32 v[14:15], v[202:203], v[202:203] op_sel:[0,1]
	v_pk_mov_b32 v[16:17], v[204:205], v[204:205] op_sel:[0,1]
	v_lshlrev_b32_e32 v20, 16, v14
	v_and_b32_e32 v21, 0xffff0000, v14
	v_lshlrev_b32_e32 v14, 16, v15
	v_and_b32_e32 v15, 0xffff0000, v15
	v_lshlrev_b32_e32 v22, 16, v16
	v_and_b32_e32 v23, 0xffff0000, v16
	v_lshlrev_b32_e32 v16, 16, v17
	v_and_b32_e32 v17, 0xffff0000, v17
	v_pk_add_f32 v[8:9], v[8:9], v[14:15]
	v_pk_add_f32 v[6:7], v[6:7], v[20:21]
	v_pk_add_f32 v[14:15], v[4:5], v[16:17]
	v_pk_add_f32 v[16:17], v[2:3], v[22:23]
	v_mul_f32_e32 v2, v7, v7
	v_mul_f32_e32 v3, v9, v9
	v_mul_f32_e32 v4, v17, v17
	v_mul_f32_e32 v5, v15, v15
	v_fmac_f32_e32 v2, v6, v6
	v_fmac_f32_e32 v3, v8, v8
	v_fmac_f32_e32 v4, v16, v16
	v_fmac_f32_e32 v5, v14, v14
	v_add_f32_e32 v2, v2, v3
	v_add_f32_e32 v3, v4, v5
	v_add_f32_e32 v2, v2, v3
	v_add_f32_e32 v2, v26, v2
	ds_bpermute_b32 v3, v122, v2
	v_cvt_pk_bf16_f32 v4, v6, v7
	v_cvt_pk_bf16_f32 v5, v8, v9
	v_cvt_pk_bf16_f32 v6, v16, v17
	v_cvt_pk_bf16_f32 v7, v14, v15
	s_waitcnt lgkmcnt(0)
	v_add_f32_e32 v2, v2, v3
	ds_bpermute_b32 v3, v116, v2
	global_store_dwordx4 v[24:25], v[4:7], off offset:256
	s_and_saveexec_b64 s[20:21], s[4:5]
	s_cbranch_execz .LBB0_575
	s_waitcnt lgkmcnt(0)
	v_add_f32_e32 v2, v2, v3
	v_fma_f32 v2, v2, s42, 0.5
	v_trunc_f32_e32 v2, v2
	v_mul_f32_e32 v3, 0x2f800000, v2
	v_floor_f32_e32 v3, v3
	v_fmac_f32_e32 v2, 0xcf800000, v3
	v_cvt_u32_f32_e32 v2, v2
	v_cvt_u32_f32_e32 v3, v3
	v_lshl_add_u64 v[4:5], v[18:19], 3, s[12:13]
	global_atomic_add_x2 v[4:5], v[2:3], off

.LBB0_650:
	s_ashr_i32 s27, s26, 31
	s_lshl_b64 s[28:29], s[26:27], 20
	s_add_u32 s28, s50, s28
	s_addc_u32 s29, s51, s29
	s_and_b64 s[30:31], s[4:5], exec
	s_cselect_b32 s27, s29, s35
	s_cselect_b32 s62, s28, s34
	s_ashr_i32 s25, s24, 31
	s_lshl_b64 s[30:31], s[24:25], 20
	s_add_u32 s30, s33, s30
	s_addc_u32 s31, s40, s31
	s_and_b64 s[38:39], s[4:5], exec
	s_cselect_b32 s25, s31, s37
	s_cselect_b32 s63, s30, s36
	s_add_u32 s34, s34, 0x80080
	s_addc_u32 s35, s35, 0
	s_add_u32 s64, s36, 0x100
	v_mov_b32_e32 v2, 0
	s_addc_u32 s65, s37, 0
	s_mov_b32 s66, -2
	v_mov_b32_e32 v3, v2
	v_pk_mov_b32 v[4:5], v[2:3], v[2:3]
	v_pk_mov_b32 v[6:7], v[2:3], v[2:3]
	v_pk_mov_b32 v[8:9], v[2:3], v[2:3]
	v_pk_mov_b32 v[10:11], v[2:3], v[2:3]
	v_pk_mov_b32 v[12:13], v[2:3], v[2:3]
	v_pk_mov_b32 v[14:15], v[2:3], v[2:3]
	v_pk_mov_b32 v[16:17], v[2:3], v[2:3]
	v_pk_mov_b32 v[18:19], v[2:3], v[2:3]
	v_pk_mov_b32 v[20:21], v[2:3], v[2:3]
	v_pk_mov_b32 v[22:23], v[2:3], v[2:3]
	v_pk_mov_b32 v[24:25], v[2:3], v[2:3]
	v_pk_mov_b32 v[26:27], v[2:3], v[2:3]
	v_pk_mov_b32 v[28:29], v[2:3], v[2:3]
	v_pk_mov_b32 v[30:31], v[2:3], v[2:3]
	v_pk_mov_b32 v[32:33], v[2:3], v[2:3]
	v_pk_mov_b32 v[34:35], v[2:3], v[2:3]
	v_pk_mov_b32 v[36:37], v[2:3], v[2:3]
	v_pk_mov_b32 v[38:39], v[2:3], v[2:3]
	v_pk_mov_b32 v[40:41], v[2:3], v[2:3]
	v_pk_mov_b32 v[42:43], v[2:3], v[2:3]
	v_pk_mov_b32 v[44:45], v[2:3], v[2:3]
	v_pk_mov_b32 v[46:47], v[2:3], v[2:3]
	v_pk_mov_b32 v[48:49], v[2:3], v[2:3]
	v_pk_mov_b32 v[50:51], v[2:3], v[2:3]
	v_pk_mov_b32 v[52:53], v[2:3], v[2:3]
	v_pk_mov_b32 v[54:55], v[2:3], v[2:3]
	v_pk_mov_b32 v[56:57], v[2:3], v[2:3]
	v_pk_mov_b32 v[58:59], v[2:3], v[2:3]
	v_pk_mov_b32 v[60:61], v[2:3], v[2:3]
	v_pk_mov_b32 v[62:63], v[2:3], v[2:3]
	v_pk_mov_b32 v[64:65], v[2:3], v[2:3]
	v_pk_mov_b32 v[66:67], v[2:3], v[2:3]
	v_pk_mov_b32 v[68:69], v[2:3], v[2:3]
	v_pk_mov_b32 v[70:71], v[2:3], v[2:3]
	v_pk_mov_b32 v[72:73], v[2:3], v[2:3]
	v_pk_mov_b32 v[74:75], v[2:3], v[2:3]
	v_pk_mov_b32 v[76:77], v[2:3], v[2:3]
	v_pk_mov_b32 v[78:79], v[2:3], v[2:3]
	v_pk_mov_b32 v[80:81], v[2:3], v[2:3]
	v_pk_mov_b32 v[82:83], v[2:3], v[2:3]
	v_pk_mov_b32 v[84:85], v[2:3], v[2:3]
	v_pk_mov_b32 v[86:87], v[2:3], v[2:3]
	v_pk_mov_b32 v[88:89], v[2:3], v[2:3]
	v_pk_mov_b32 v[90:91], v[2:3], v[2:3]
	v_pk_mov_b32 v[92:93], v[2:3], v[2:3]
	v_pk_mov_b32 v[94:95], v[2:3], v[2:3]
	v_pk_mov_b32 v[96:97], v[2:3], v[2:3]
	v_pk_mov_b32 v[98:99], v[2:3], v[2:3]
	v_pk_mov_b32 v[100:101], v[2:3], v[2:3]
	v_pk_mov_b32 v[102:103], v[2:3], v[2:3]
	v_pk_mov_b32 v[104:105], v[2:3], v[2:3]
	v_pk_mov_b32 v[106:107], v[2:3], v[2:3]
	v_pk_mov_b32 v[108:109], v[2:3], v[2:3]
	v_pk_mov_b32 v[110:111], v[2:3], v[2:3]
	v_pk_mov_b32 v[112:113], v[2:3], v[2:3]
	v_pk_mov_b32 v[114:115], v[2:3], v[2:3]
	v_pk_mov_b32 v[116:117], v[2:3], v[2:3]
	v_pk_mov_b32 v[118:119], v[2:3], v[2:3]
	v_pk_mov_b32 v[120:121], v[2:3], v[2:3]
	v_pk_mov_b32 v[122:123], v[2:3], v[2:3]
	v_pk_mov_b32 v[124:125], v[2:3], v[2:3]
	v_pk_mov_b32 v[126:127], v[2:3], v[2:3]
	v_pk_mov_b32 v[128:129], v[2:3], v[2:3]

.LBB0_847:
	s_ashr_i32 s23, s22, 31
	s_lshl_b64 s[24:25], s[22:23], 20
	s_add_u32 s24, s70, s24
	s_addc_u32 s25, s71, s25
	s_and_b64 s[26:27], s[4:5], exec
	s_cselect_b32 s23, s25, s35
	s_cselect_b32 s58, s24, s34
	s_ashr_i32 s21, s20, 31
	s_lshl_b64 s[26:27], s[20:21], 20
	s_add_u32 s26, s33, s26
	s_addc_u32 s27, s40, s27
	s_and_b64 s[38:39], s[4:5], exec
	s_cselect_b32 s21, s27, s37
	s_cselect_b32 s59, s26, s36
	s_add_u32 s34, s34, 0x80080
	s_addc_u32 s35, s35, 0
	s_add_u32 s60, s36, 0x100
	v_mov_b32_e32 v2, 0
	s_addc_u32 s61, s37, 0
	s_mov_b32 s62, -2
	v_mov_b32_e32 v3, v2
	v_pk_mov_b32 v[4:5], v[2:3], v[2:3]
	v_pk_mov_b32 v[6:7], v[2:3], v[2:3]
	v_pk_mov_b32 v[8:9], v[2:3], v[2:3]
	v_pk_mov_b32 v[10:11], v[2:3], v[2:3]
	v_pk_mov_b32 v[12:13], v[2:3], v[2:3]
	v_pk_mov_b32 v[14:15], v[2:3], v[2:3]
	v_pk_mov_b32 v[16:17], v[2:3], v[2:3]
	v_pk_mov_b32 v[18:19], v[2:3], v[2:3]
	v_pk_mov_b32 v[20:21], v[2:3], v[2:3]
	v_pk_mov_b32 v[22:23], v[2:3], v[2:3]
	v_pk_mov_b32 v[24:25], v[2:3], v[2:3]
	v_pk_mov_b32 v[26:27], v[2:3], v[2:3]
	v_pk_mov_b32 v[28:29], v[2:3], v[2:3]
	v_pk_mov_b32 v[30:31], v[2:3], v[2:3]
	v_pk_mov_b32 v[32:33], v[2:3], v[2:3]
	v_pk_mov_b32 v[34:35], v[2:3], v[2:3]
	v_pk_mov_b32 v[36:37], v[2:3], v[2:3]
	v_pk_mov_b32 v[38:39], v[2:3], v[2:3]
	v_pk_mov_b32 v[40:41], v[2:3], v[2:3]
	v_pk_mov_b32 v[42:43], v[2:3], v[2:3]
	v_pk_mov_b32 v[44:45], v[2:3], v[2:3]
	v_pk_mov_b32 v[46:47], v[2:3], v[2:3]
	v_pk_mov_b32 v[48:49], v[2:3], v[2:3]
	v_pk_mov_b32 v[50:51], v[2:3], v[2:3]
	v_pk_mov_b32 v[52:53], v[2:3], v[2:3]
	v_pk_mov_b32 v[54:55], v[2:3], v[2:3]
	v_pk_mov_b32 v[56:57], v[2:3], v[2:3]
	v_pk_mov_b32 v[58:59], v[2:3], v[2:3]
	v_pk_mov_b32 v[60:61], v[2:3], v[2:3]
	v_pk_mov_b32 v[62:63], v[2:3], v[2:3]
	v_pk_mov_b32 v[64:65], v[2:3], v[2:3]
	v_pk_mov_b32 v[66:67], v[2:3], v[2:3]
	v_pk_mov_b32 v[68:69], v[2:3], v[2:3]
	v_pk_mov_b32 v[70:71], v[2:3], v[2:3]
	v_pk_mov_b32 v[72:73], v[2:3], v[2:3]
	v_pk_mov_b32 v[74:75], v[2:3], v[2:3]
	v_pk_mov_b32 v[76:77], v[2:3], v[2:3]
	v_pk_mov_b32 v[78:79], v[2:3], v[2:3]
	v_pk_mov_b32 v[80:81], v[2:3], v[2:3]
	v_pk_mov_b32 v[82:83], v[2:3], v[2:3]
	v_pk_mov_b32 v[84:85], v[2:3], v[2:3]
	v_pk_mov_b32 v[86:87], v[2:3], v[2:3]
	v_pk_mov_b32 v[88:89], v[2:3], v[2:3]
	v_pk_mov_b32 v[90:91], v[2:3], v[2:3]
	v_pk_mov_b32 v[92:93], v[2:3], v[2:3]
	v_pk_mov_b32 v[94:95], v[2:3], v[2:3]
	v_pk_mov_b32 v[96:97], v[2:3], v[2:3]
	v_pk_mov_b32 v[98:99], v[2:3], v[2:3]
	v_pk_mov_b32 v[100:101], v[2:3], v[2:3]
	v_pk_mov_b32 v[102:103], v[2:3], v[2:3]
	v_pk_mov_b32 v[104:105], v[2:3], v[2:3]
	v_pk_mov_b32 v[106:107], v[2:3], v[2:3]
	v_pk_mov_b32 v[108:109], v[2:3], v[2:3]
	v_pk_mov_b32 v[110:111], v[2:3], v[2:3]
	v_pk_mov_b32 v[112:113], v[2:3], v[2:3]
	v_pk_mov_b32 v[114:115], v[2:3], v[2:3]
	v_pk_mov_b32 v[116:117], v[2:3], v[2:3]
	v_pk_mov_b32 v[118:119], v[2:3], v[2:3]
	v_pk_mov_b32 v[120:121], v[2:3], v[2:3]
	v_pk_mov_b32 v[122:123], v[2:3], v[2:3]
	v_pk_mov_b32 v[124:125], v[2:3], v[2:3]
	v_pk_mov_b32 v[126:127], v[2:3], v[2:3]
	v_pk_mov_b32 v[128:129], v[2:3], v[2:3]

.LBB0_851:
	v_lshl_add_u32 v152, s30, 8, v154
	v_lshl_or_b32 v150, s57, 8, v156
	v_ashrrev_i32_e32 v153, 31, v152
	v_ashrrev_i32_e32 v151, 31, v150
	v_lshlrev_b64 v[148:149], 11, v[152:153]
	v_lshl_add_u64 v[148:149], v[148:149], 0, v[150:151]
	v_lshl_add_u64 v[166:167], v[148:149], 1, s[50:51]
	v_mov_b32_e32 v222, v166
	v_mov_b32_e32 v223, v167
	v_mov_b32_e32 v240, 0x10000
	v_mov_b32_e32 v241, 0
	global_load_dwordx4 v[174:177], v[222:223], off
	global_load_dwordx4 v[178:181], v[222:223], off offset:256
	v_lshl_add_u64 v[222:223], v[240:241], 0, v[222:223]
	global_load_dwordx4 v[182:185], v[222:223], off
	global_load_dwordx4 v[186:189], v[222:223], off offset:256
	v_lshl_add_u64 v[222:223], v[240:241], 0, v[222:223]
	global_load_dwordx4 v[190:193], v[222:223], off
	global_load_dwordx4 v[194:197], v[222:223], off offset:256
	v_lshl_add_u64 v[222:223], v[240:241], 0, v[222:223]
	global_load_dwordx4 v[198:201], v[222:223], off
	global_load_dwordx4 v[202:205], v[222:223], off offset:256
	v_lshl_add_u64 v[222:223], v[240:241], 2, v[222:223]
	v_lshl_add_u64 v[222:223], v[240:241], 0, v[222:223]
	global_load_dwordx4 v[206:209], v[222:223], off
	global_load_dwordx4 v[210:213], v[222:223], off offset:256
	v_lshl_add_u64 v[222:223], v[240:241], 0, v[222:223]
	global_load_dwordx4 v[214:217], v[222:223], off
	global_load_dwordx4 v[218:221], v[222:223], off offset:256
	s_nop 0
	v_lshl_add_u64 v[168:169], v[148:149], 2, s[28:29]
	s_andn2_b64 vcc, exec, s[4:5]
	s_mov_b64 s[4:5], -1
	s_waitcnt vmcnt(10)
	s_nop 1
	v_pk_mov_b32 v[162:163], v[174:175], v[174:175] op_sel:[0,1]
	v_pk_mov_b32 v[164:165], v[176:177], v[176:177] op_sel:[0,1]
	v_lshlrev_b32_e32 v170, 16, v162
	v_and_b32_e32 v171, 0xffff0000, v162
	v_lshlrev_b32_e32 v162, 16, v163
	v_and_b32_e32 v163, 0xffff0000, v163
	v_lshlrev_b32_e32 v172, 16, v164
	v_and_b32_e32 v173, 0xffff0000, v164
	v_lshlrev_b32_e32 v164, 16, v165
	v_and_b32_e32 v165, 0xffff0000, v165
	v_pk_add_f32 v[128:129], v[128:129], v[162:163]
	v_pk_add_f32 v[126:127], v[126:127], v[170:171]
	v_pk_add_f32 v[124:125], v[124:125], v[164:165]
	v_pk_add_f32 v[122:123], v[122:123], v[172:173]
	global_store_dwordx4 v[168:169], v[126:129], off
	global_store_dwordx4 v[168:169], v[122:125], off offset:16
	s_nop 0
	v_or_b32_e32 v126, 16, v152
	v_ashrrev_i32_e32 v127, 31, v126
	v_lshlrev_b64 v[126:127], 11, v[126:127]
	v_lshl_add_u64 v[126:127], v[126:127], 0, v[150:151]
	v_lshl_add_u64 v[128:129], v[126:127], 1, s[50:51]
	s_nop 1
	v_pk_mov_b32 v[122:123], v[178:179], v[178:179] op_sel:[0,1]
	v_pk_mov_b32 v[124:125], v[180:181], v[180:181] op_sel:[0,1]
	v_lshl_add_u64 v[222:223], v[240:241], 0, v[222:223]
	global_load_dwordx4 v[174:177], v[222:223], off
	global_load_dwordx4 v[178:181], v[222:223], off offset:256
	v_lshlrev_b32_e32 v162, 16, v122
	v_and_b32_e32 v163, 0xffff0000, v122
	v_lshlrev_b32_e32 v122, 16, v123
	v_and_b32_e32 v123, 0xffff0000, v123
	v_lshlrev_b32_e32 v164, 16, v124
	v_and_b32_e32 v165, 0xffff0000, v124
	v_lshlrev_b32_e32 v124, 16, v125
	v_and_b32_e32 v125, 0xffff0000, v125
	v_pk_add_f32 v[120:121], v[120:121], v[122:123]
	v_pk_add_f32 v[118:119], v[118:119], v[162:163]
	v_pk_add_f32 v[116:117], v[116:117], v[124:125]
	v_pk_add_f32 v[114:115], v[114:115], v[164:165]
	global_store_dwordx4 v[168:169], v[118:121], off offset:512
	global_store_dwordx4 v[168:169], v[114:117], off offset:528
	s_nop 0
	v_lshl_add_u64 v[118:119], v[126:127], 2, s[28:29]
	s_waitcnt vmcnt(14)
	s_nop 1
	v_pk_mov_b32 v[114:115], v[182:183], v[182:183] op_sel:[0,1]
	v_pk_mov_b32 v[116:117], v[184:185], v[184:185] op_sel:[0,1]
	v_lshlrev_b32_e32 v120, 16, v114
	v_and_b32_e32 v121, 0xffff0000, v114
	v_lshlrev_b32_e32 v114, 16, v115
	v_and_b32_e32 v115, 0xffff0000, v115
	v_lshlrev_b32_e32 v122, 16, v116
	v_and_b32_e32 v123, 0xffff0000, v116
	v_lshlrev_b32_e32 v116, 16, v117
	v_and_b32_e32 v117, 0xffff0000, v117
	v_pk_add_f32 v[112:113], v[112:113], v[114:115]
	v_pk_add_f32 v[110:111], v[110:111], v[120:121]
	v_pk_add_f32 v[108:109], v[108:109], v[116:117]
	v_pk_add_f32 v[106:107], v[106:107], v[122:123]
	global_store_dwordx4 v[118:119], v[110:113], off
	global_store_dwordx4 v[118:119], v[106:109], off offset:16
	s_nop 0
	v_or_b32_e32 v110, 32, v152
	v_ashrrev_i32_e32 v111, 31, v110
	v_lshlrev_b64 v[110:111], 11, v[110:111]
	v_lshl_add_u64 v[110:111], v[110:111], 0, v[150:151]
	v_lshl_add_u64 v[112:113], v[110:111], 1, s[50:51]
	s_nop 1
	v_pk_mov_b32 v[106:107], v[186:187], v[186:187] op_sel:[0,1]
	v_pk_mov_b32 v[108:109], v[188:189], v[188:189] op_sel:[0,1]
	v_lshl_add_u64 v[222:223], v[240:241], 0, v[222:223]
	global_load_dwordx4 v[182:185], v[222:223], off
	global_load_dwordx4 v[186:189], v[222:223], off offset:256
	v_lshlrev_b32_e32 v114, 16, v106
	v_and_b32_e32 v115, 0xffff0000, v106
	v_lshlrev_b32_e32 v106, 16, v107
	v_and_b32_e32 v107, 0xffff0000, v107
	v_lshlrev_b32_e32 v116, 16, v108
	v_and_b32_e32 v117, 0xffff0000, v108
	v_lshlrev_b32_e32 v108, 16, v109
	v_and_b32_e32 v109, 0xffff0000, v109
	v_pk_add_f32 v[104:105], v[104:105], v[106:107]
	v_pk_add_f32 v[102:103], v[102:103], v[114:115]
	v_pk_add_f32 v[100:101], v[100:101], v[108:109]
	v_pk_add_f32 v[98:99], v[98:99], v[116:117]
	global_store_dwordx4 v[118:119], v[102:105], off offset:512
	global_store_dwordx4 v[118:119], v[98:101], off offset:528
	s_nop 0
	v_lshl_add_u64 v[102:103], v[110:111], 2, s[28:29]
	s_waitcnt vmcnt(18)
	s_nop 1
	v_pk_mov_b32 v[98:99], v[190:191], v[190:191] op_sel:[0,1]
	v_pk_mov_b32 v[100:101], v[192:193], v[192:193] op_sel:[0,1]
	v_lshlrev_b32_e32 v104, 16, v98
	v_and_b32_e32 v105, 0xffff0000, v98
	v_lshlrev_b32_e32 v98, 16, v99
	v_and_b32_e32 v99, 0xffff0000, v99
	v_lshlrev_b32_e32 v106, 16, v100
	v_and_b32_e32 v107, 0xffff0000, v100
	v_lshlrev_b32_e32 v100, 16, v101
	v_and_b32_e32 v101, 0xffff0000, v101
	v_pk_add_f32 v[96:97], v[96:97], v[98:99]
	v_pk_add_f32 v[94:95], v[94:95], v[104:105]
	v_pk_add_f32 v[92:93], v[92:93], v[100:101]
	v_pk_add_f32 v[90:91], v[90:91], v[106:107]
	global_store_dwordx4 v[102:103], v[94:97], off
	global_store_dwordx4 v[102:103], v[90:93], off offset:16
	s_nop 0
	v_or_b32_e32 v94, 48, v152
	v_ashrrev_i32_e32 v95, 31, v94
	v_lshlrev_b64 v[94:95], 11, v[94:95]
	v_lshl_add_u64 v[94:95], v[94:95], 0, v[150:151]
	v_lshl_add_u64 v[96:97], v[94:95], 1, s[50:51]
	s_nop 1
	v_pk_mov_b32 v[90:91], v[194:195], v[194:195] op_sel:[0,1]
	v_pk_mov_b32 v[92:93], v[196:197], v[196:197] op_sel:[0,1]
	v_lshlrev_b32_e32 v98, 16, v90
	v_and_b32_e32 v99, 0xffff0000, v90
	v_lshlrev_b32_e32 v90, 16, v91
	v_and_b32_e32 v91, 0xffff0000, v91
	v_lshlrev_b32_e32 v100, 16, v92
	v_and_b32_e32 v101, 0xffff0000, v92
	v_lshlrev_b32_e32 v92, 16, v93
	v_and_b32_e32 v93, 0xffff0000, v93
	v_pk_add_f32 v[88:89], v[88:89], v[90:91]
	v_pk_add_f32 v[86:87], v[86:87], v[98:99]
	v_pk_add_f32 v[84:85], v[84:85], v[92:93]
	v_pk_add_f32 v[82:83], v[82:83], v[100:101]
	global_store_dwordx4 v[102:103], v[86:89], off offset:512
	global_store_dwordx4 v[102:103], v[82:85], off offset:528
	s_nop 0
	v_lshl_add_u64 v[86:87], v[94:95], 2, s[28:29]
	s_waitcnt vmcnt(20)
	s_nop 1
	v_pk_mov_b32 v[82:83], v[198:199], v[198:199] op_sel:[0,1]
	v_pk_mov_b32 v[84:85], v[200:201], v[200:201] op_sel:[0,1]
	v_lshlrev_b32_e32 v88, 16, v82
	v_and_b32_e32 v89, 0xffff0000, v82
	v_lshlrev_b32_e32 v82, 16, v83
	v_and_b32_e32 v83, 0xffff0000, v83
	v_lshlrev_b32_e32 v90, 16, v84
	v_and_b32_e32 v91, 0xffff0000, v84
	v_lshlrev_b32_e32 v84, 16, v85
	v_and_b32_e32 v85, 0xffff0000, v85
	v_pk_add_f32 v[80:81], v[80:81], v[82:83]
	v_pk_add_f32 v[78:79], v[78:79], v[88:89]
	v_pk_add_f32 v[76:77], v[76:77], v[84:85]
	v_pk_add_f32 v[74:75], v[74:75], v[90:91]
	global_store_dwordx4 v[86:87], v[78:81], off
	global_store_dwordx4 v[86:87], v[74:77], off offset:16
	s_nop 0
	v_lshl_add_u64 v[78:79], v[148:149], 0, s[12:13]
	v_lshl_add_u64 v[80:81], v[78:79], 1, s[50:51]
	s_nop 1
	v_pk_mov_b32 v[74:75], v[202:203], v[202:203] op_sel:[0,1]
	v_pk_mov_b32 v[76:77], v[204:205], v[204:205] op_sel:[0,1]
	v_lshlrev_b32_e32 v82, 16, v74
	v_and_b32_e32 v83, 0xffff0000, v74
	v_lshlrev_b32_e32 v74, 16, v75
	v_and_b32_e32 v75, 0xffff0000, v75
	v_lshlrev_b32_e32 v84, 16, v76
	v_and_b32_e32 v85, 0xffff0000, v76
	v_lshlrev_b32_e32 v76, 16, v77
	v_and_b32_e32 v77, 0xffff0000, v77
	v_pk_add_f32 v[72:73], v[72:73], v[74:75]
	v_pk_add_f32 v[70:71], v[70:71], v[82:83]
	v_pk_add_f32 v[68:69], v[68:69], v[76:77]
	v_pk_add_f32 v[66:67], v[66:67], v[84:85]
	global_store_dwordx4 v[86:87], v[70:73], off offset:512
	global_store_dwordx4 v[86:87], v[66:69], off offset:528
	s_nop 0
	v_lshl_add_u64 v[70:71], v[78:79], 2, s[28:29]
	s_waitcnt vmcnt(22)
	s_nop 1
	v_pk_mov_b32 v[66:67], v[206:207], v[206:207] op_sel:[0,1]
	v_pk_mov_b32 v[68:69], v[208:209], v[208:209] op_sel:[0,1]
	v_lshlrev_b32_e32 v72, 16, v66
	v_and_b32_e32 v73, 0xffff0000, v66
	v_lshlrev_b32_e32 v66, 16, v67
	v_and_b32_e32 v67, 0xffff0000, v67
	v_lshlrev_b32_e32 v74, 16, v68
	v_and_b32_e32 v75, 0xffff0000, v68
	v_lshlrev_b32_e32 v68, 16, v69
	v_and_b32_e32 v69, 0xffff0000, v69
	v_pk_add_f32 v[64:65], v[64:65], v[66:67]
	v_pk_add_f32 v[62:63], v[62:63], v[72:73]
	v_pk_add_f32 v[60:61], v[60:61], v[68:69]
	v_pk_add_f32 v[58:59], v[58:59], v[74:75]
	global_store_dwordx4 v[70:71], v[62:65], off
	global_store_dwordx4 v[70:71], v[58:61], off offset:16
	s_nop 0
	v_lshl_add_u64 v[62:63], v[148:149], 0, s[14:15]
	v_lshl_add_u64 v[64:65], v[62:63], 1, s[50:51]
	s_nop 1
	v_pk_mov_b32 v[58:59], v[210:211], v[210:211] op_sel:[0,1]
	v_pk_mov_b32 v[60:61], v[212:213], v[212:213] op_sel:[0,1]
	v_lshlrev_b32_e32 v66, 16, v58
	v_and_b32_e32 v67, 0xffff0000, v58
	v_lshlrev_b32_e32 v58, 16, v59
	v_and_b32_e32 v59, 0xffff0000, v59
	v_lshlrev_b32_e32 v68, 16, v60
	v_and_b32_e32 v69, 0xffff0000, v60
	v_lshlrev_b32_e32 v60, 16, v61
	v_and_b32_e32 v61, 0xffff0000, v61
	v_pk_add_f32 v[56:57], v[56:57], v[58:59]
	v_pk_add_f32 v[54:55], v[54:55], v[66:67]
	v_pk_add_f32 v[52:53], v[52:53], v[60:61]
	v_pk_add_f32 v[50:51], v[50:51], v[68:69]
	global_store_dwordx4 v[70:71], v[54:57], off offset:512
	global_store_dwordx4 v[70:71], v[50:53], off offset:528
	s_nop 0
	v_lshl_add_u64 v[54:55], v[62:63], 2, s[28:29]
	s_waitcnt vmcnt(24)
	s_nop 1
	v_pk_mov_b32 v[50:51], v[214:215], v[214:215] op_sel:[0,1]
	v_pk_mov_b32 v[52:53], v[216:217], v[216:217] op_sel:[0,1]
	v_lshlrev_b32_e32 v56, 16, v50
	v_and_b32_e32 v57, 0xffff0000, v50
	v_lshlrev_b32_e32 v50, 16, v51
	v_and_b32_e32 v51, 0xffff0000, v51
	v_lshlrev_b32_e32 v58, 16, v52
	v_and_b32_e32 v59, 0xffff0000, v52
	v_lshlrev_b32_e32 v52, 16, v53
	v_and_b32_e32 v53, 0xffff0000, v53
	v_pk_add_f32 v[48:49], v[48:49], v[50:51]
	v_pk_add_f32 v[46:47], v[46:47], v[56:57]
	v_pk_add_f32 v[44:45], v[44:45], v[52:53]
	v_pk_add_f32 v[42:43], v[42:43], v[58:59]
	global_store_dwordx4 v[54:55], v[46:49], off
	global_store_dwordx4 v[54:55], v[42:45], off offset:16
	s_nop 0
	v_lshl_add_u64 v[46:47], v[148:149], 0, s[16:17]
	v_lshl_add_u64 v[48:49], v[46:47], 1, s[50:51]
	s_nop 1
	v_pk_mov_b32 v[42:43], v[218:219], v[218:219] op_sel:[0,1]
	v_pk_mov_b32 v[44:45], v[220:221], v[220:221] op_sel:[0,1]
	v_lshlrev_b32_e32 v50, 16, v42
	v_and_b32_e32 v51, 0xffff0000, v42
	v_lshlrev_b32_e32 v42, 16, v43
	v_and_b32_e32 v43, 0xffff0000, v43
	v_lshlrev_b32_e32 v52, 16, v44
	v_and_b32_e32 v53, 0xffff0000, v44
	v_lshlrev_b32_e32 v44, 16, v45
	v_and_b32_e32 v45, 0xffff0000, v45
	v_pk_add_f32 v[40:41], v[40:41], v[42:43]
	v_pk_add_f32 v[38:39], v[38:39], v[50:51]
	v_pk_add_f32 v[36:37], v[36:37], v[44:45]
	v_pk_add_f32 v[34:35], v[34:35], v[52:53]
	global_store_dwordx4 v[54:55], v[38:41], off offset:512
	global_store_dwordx4 v[54:55], v[34:37], off offset:528
	s_nop 0
	v_lshl_add_u64 v[38:39], v[46:47], 2, s[28:29]
	s_waitcnt vmcnt(24)
	s_nop 1
	v_pk_mov_b32 v[34:35], v[174:175], v[174:175] op_sel:[0,1]
	v_pk_mov_b32 v[36:37], v[176:177], v[176:177] op_sel:[0,1]
	v_lshlrev_b32_e32 v40, 16, v34
	v_and_b32_e32 v41, 0xffff0000, v34
	v_lshlrev_b32_e32 v34, 16, v35
	v_and_b32_e32 v35, 0xffff0000, v35
	v_lshlrev_b32_e32 v42, 16, v36
	v_and_b32_e32 v43, 0xffff0000, v36
	v_lshlrev_b32_e32 v36, 16, v37
	v_and_b32_e32 v37, 0xffff0000, v37
	v_pk_add_f32 v[32:33], v[32:33], v[34:35]
	v_pk_add_f32 v[30:31], v[30:31], v[40:41]
	v_pk_add_f32 v[28:29], v[28:29], v[36:37]
	v_pk_add_f32 v[26:27], v[26:27], v[42:43]
	global_store_dwordx4 v[38:39], v[30:33], off
	global_store_dwordx4 v[38:39], v[26:29], off offset:16
	s_nop 0
	v_lshl_add_u64 v[30:31], v[148:149], 0, s[18:19]
	v_lshl_add_u64 v[32:33], v[30:31], 1, s[50:51]
	s_nop 1
	v_pk_mov_b32 v[26:27], v[178:179], v[178:179] op_sel:[0,1]
	v_pk_mov_b32 v[28:29], v[180:181], v[180:181] op_sel:[0,1]
	v_lshlrev_b32_e32 v34, 16, v26
	v_and_b32_e32 v35, 0xffff0000, v26
	v_lshlrev_b32_e32 v26, 16, v27
	v_and_b32_e32 v27, 0xffff0000, v27
	v_lshlrev_b32_e32 v36, 16, v28
	v_and_b32_e32 v37, 0xffff0000, v28
	v_lshlrev_b32_e32 v28, 16, v29
	v_and_b32_e32 v29, 0xffff0000, v29
	v_pk_add_f32 v[24:25], v[24:25], v[26:27]
	v_pk_add_f32 v[22:23], v[22:23], v[34:35]
	v_pk_add_f32 v[20:21], v[20:21], v[28:29]
	v_pk_add_f32 v[18:19], v[18:19], v[36:37]
	global_store_dwordx4 v[38:39], v[22:25], off offset:512
	global_store_dwordx4 v[38:39], v[18:21], off offset:528
	s_nop 0
	v_lshl_add_u64 v[22:23], v[30:31], 2, s[28:29]
	s_waitcnt vmcnt(22)
	s_nop 1
	v_pk_mov_b32 v[18:19], v[182:183], v[182:183] op_sel:[0,1]
	v_pk_mov_b32 v[20:21], v[184:185], v[184:185] op_sel:[0,1]
	v_lshlrev_b32_e32 v24, 16, v18
	v_and_b32_e32 v25, 0xffff0000, v18
	v_lshlrev_b32_e32 v18, 16, v19
	v_and_b32_e32 v19, 0xffff0000, v19
	v_lshlrev_b32_e32 v26, 16, v20
	v_and_b32_e32 v27, 0xffff0000, v20
	v_lshlrev_b32_e32 v20, 16, v21
	v_and_b32_e32 v21, 0xffff0000, v21
	v_pk_add_f32 v[16:17], v[16:17], v[18:19]
	v_pk_add_f32 v[14:15], v[14:15], v[24:25]
	v_pk_add_f32 v[12:13], v[12:13], v[20:21]
	v_pk_add_f32 v[10:11], v[10:11], v[26:27]
	global_store_dwordx4 v[22:23], v[14:17], off
	global_store_dwordx4 v[22:23], v[10:13], off offset:16
	s_nop 0
	s_nop 1
	v_pk_mov_b32 v[10:11], v[186:187], v[186:187] op_sel:[0,1]
	v_pk_mov_b32 v[12:13], v[188:189], v[188:189] op_sel:[0,1]
	v_lshlrev_b32_e32 v14, 16, v10
	v_and_b32_e32 v15, 0xffff0000, v10
	v_lshlrev_b32_e32 v10, 16, v11
	v_and_b32_e32 v11, 0xffff0000, v11
	v_lshlrev_b32_e32 v16, 16, v12
	v_and_b32_e32 v17, 0xffff0000, v12
	v_lshlrev_b32_e32 v12, 16, v13
	v_and_b32_e32 v13, 0xffff0000, v13
	v_pk_add_f32 v[8:9], v[8:9], v[10:11]
	v_pk_add_f32 v[6:7], v[6:7], v[14:15]
	v_pk_add_f32 v[4:5], v[4:5], v[12:13]
	v_pk_add_f32 v[2:3], v[2:3], v[16:17]
	global_store_dwordx4 v[22:23], v[6:9], off offset:512
	global_store_dwordx4 v[22:23], v[2:5], off offset:528
	s_cbranch_vccnz .LBB0_840
	s_andn2_b64 vcc, exec, s[6:7]
	s_cbranch_vccnz .LBB0_839
	s_barrier
	s_branch .LBB0_839

.LBB0_1083:
	s_lshl_b64 s[20:21], s[16:17], 19
	s_add_u32 s20, s15, s20
	s_addc_u32 s21, s33, s21
	s_and_b64 s[22:23], exec, s[2:3]
	s_cselect_b32 s17, s21, s27
	s_cselect_b32 s59, s20, s26
	s_ashr_i32 s19, s18, 31
	s_lshl_b64 s[22:23], s[18:19], 19
	s_add_u32 s22, s36, s22
	s_addc_u32 s23, s37, s23
	s_and_b64 s[34:35], exec, s[2:3]
	s_cselect_b32 s19, s23, s31
	s_cselect_b32 s60, s22, s30
	s_add_u32 s26, s26, 0x40080
	s_addc_u32 s27, s27, 0
	s_add_u32 s61, s30, 0x100
	v_mov_b32_e32 v2, 0
	s_addc_u32 s62, s31, 0
	s_mov_b32 s63, -2
	v_mov_b32_e32 v3, v2
	v_pk_mov_b32 v[4:5], v[2:3], v[2:3]
	v_pk_mov_b32 v[6:7], v[2:3], v[2:3]
	v_pk_mov_b32 v[8:9], v[2:3], v[2:3]
	v_pk_mov_b32 v[10:11], v[2:3], v[2:3]
	v_pk_mov_b32 v[12:13], v[2:3], v[2:3]
	v_pk_mov_b32 v[14:15], v[2:3], v[2:3]
	v_pk_mov_b32 v[16:17], v[2:3], v[2:3]
	v_pk_mov_b32 v[18:19], v[2:3], v[2:3]
	v_pk_mov_b32 v[20:21], v[2:3], v[2:3]
	v_pk_mov_b32 v[22:23], v[2:3], v[2:3]
	v_pk_mov_b32 v[24:25], v[2:3], v[2:3]
	v_pk_mov_b32 v[26:27], v[2:3], v[2:3]
	v_pk_mov_b32 v[28:29], v[2:3], v[2:3]
	v_pk_mov_b32 v[30:31], v[2:3], v[2:3]
	v_pk_mov_b32 v[32:33], v[2:3], v[2:3]
	v_pk_mov_b32 v[34:35], v[2:3], v[2:3]
	v_pk_mov_b32 v[36:37], v[2:3], v[2:3]
	v_pk_mov_b32 v[38:39], v[2:3], v[2:3]
	v_pk_mov_b32 v[40:41], v[2:3], v[2:3]
	v_pk_mov_b32 v[42:43], v[2:3], v[2:3]
	v_pk_mov_b32 v[44:45], v[2:3], v[2:3]
	v_pk_mov_b32 v[46:47], v[2:3], v[2:3]
	v_pk_mov_b32 v[48:49], v[2:3], v[2:3]
	v_pk_mov_b32 v[50:51], v[2:3], v[2:3]
	v_pk_mov_b32 v[52:53], v[2:3], v[2:3]
	v_pk_mov_b32 v[54:55], v[2:3], v[2:3]
	v_pk_mov_b32 v[56:57], v[2:3], v[2:3]
	v_pk_mov_b32 v[58:59], v[2:3], v[2:3]
	v_pk_mov_b32 v[60:61], v[2:3], v[2:3]
	v_pk_mov_b32 v[62:63], v[2:3], v[2:3]
	v_pk_mov_b32 v[64:65], v[2:3], v[2:3]
	v_pk_mov_b32 v[66:67], v[2:3], v[2:3]
	v_pk_mov_b32 v[68:69], v[2:3], v[2:3]
	v_pk_mov_b32 v[70:71], v[2:3], v[2:3]
	v_pk_mov_b32 v[72:73], v[2:3], v[2:3]
	v_pk_mov_b32 v[74:75], v[2:3], v[2:3]
	v_pk_mov_b32 v[76:77], v[2:3], v[2:3]
	v_pk_mov_b32 v[78:79], v[2:3], v[2:3]
	v_pk_mov_b32 v[80:81], v[2:3], v[2:3]
	v_pk_mov_b32 v[82:83], v[2:3], v[2:3]
	v_pk_mov_b32 v[84:85], v[2:3], v[2:3]
	v_pk_mov_b32 v[86:87], v[2:3], v[2:3]
	v_pk_mov_b32 v[88:89], v[2:3], v[2:3]
	v_pk_mov_b32 v[90:91], v[2:3], v[2:3]
	v_pk_mov_b32 v[92:93], v[2:3], v[2:3]
	v_pk_mov_b32 v[94:95], v[2:3], v[2:3]
	v_pk_mov_b32 v[96:97], v[2:3], v[2:3]
	v_pk_mov_b32 v[98:99], v[2:3], v[2:3]
	v_pk_mov_b32 v[100:101], v[2:3], v[2:3]
	v_pk_mov_b32 v[102:103], v[2:3], v[2:3]
	v_pk_mov_b32 v[104:105], v[2:3], v[2:3]
	v_pk_mov_b32 v[106:107], v[2:3], v[2:3]
	v_pk_mov_b32 v[108:109], v[2:3], v[2:3]
	v_pk_mov_b32 v[110:111], v[2:3], v[2:3]
	v_pk_mov_b32 v[112:113], v[2:3], v[2:3]
	v_pk_mov_b32 v[114:115], v[2:3], v[2:3]
	v_pk_mov_b32 v[116:117], v[2:3], v[2:3]
	v_pk_mov_b32 v[118:119], v[2:3], v[2:3]
	v_pk_mov_b32 v[120:121], v[2:3], v[2:3]
	v_pk_mov_b32 v[122:123], v[2:3], v[2:3]
	v_pk_mov_b32 v[124:125], v[2:3], v[2:3]
	v_pk_mov_b32 v[126:127], v[2:3], v[2:3]
	v_pk_mov_b32 v[128:129], v[2:3], v[2:3]

.LBB0_1158:
	s_add_u32 s36, s36, 0xe0080
	s_addc_u32 s37, s37, 0
	s_add_u32 s1, s38, 0x100
	v_mov_b32_e32 v2, 0
	s_addc_u32 s68, s39, 0
	s_mov_b32 s69, -2
	v_mov_b32_e32 v3, v2
	v_pk_mov_b32 v[4:5], v[2:3], v[2:3]
	v_pk_mov_b32 v[6:7], v[2:3], v[2:3]
	v_pk_mov_b32 v[8:9], v[2:3], v[2:3]
	v_pk_mov_b32 v[10:11], v[2:3], v[2:3]
	v_pk_mov_b32 v[12:13], v[2:3], v[2:3]
	v_pk_mov_b32 v[14:15], v[2:3], v[2:3]
	v_pk_mov_b32 v[16:17], v[2:3], v[2:3]
	v_pk_mov_b32 v[18:19], v[2:3], v[2:3]
	v_pk_mov_b32 v[20:21], v[2:3], v[2:3]
	v_pk_mov_b32 v[22:23], v[2:3], v[2:3]
	v_pk_mov_b32 v[24:25], v[2:3], v[2:3]
	v_pk_mov_b32 v[26:27], v[2:3], v[2:3]
	v_pk_mov_b32 v[28:29], v[2:3], v[2:3]
	v_pk_mov_b32 v[30:31], v[2:3], v[2:3]
	v_pk_mov_b32 v[32:33], v[2:3], v[2:3]
	v_pk_mov_b32 v[34:35], v[2:3], v[2:3]
	v_pk_mov_b32 v[36:37], v[2:3], v[2:3]
	v_pk_mov_b32 v[38:39], v[2:3], v[2:3]
	v_pk_mov_b32 v[40:41], v[2:3], v[2:3]
	v_pk_mov_b32 v[42:43], v[2:3], v[2:3]
	v_pk_mov_b32 v[44:45], v[2:3], v[2:3]
	v_pk_mov_b32 v[46:47], v[2:3], v[2:3]
	v_pk_mov_b32 v[48:49], v[2:3], v[2:3]
	v_pk_mov_b32 v[50:51], v[2:3], v[2:3]
	v_pk_mov_b32 v[52:53], v[2:3], v[2:3]
	v_pk_mov_b32 v[54:55], v[2:3], v[2:3]
	v_pk_mov_b32 v[56:57], v[2:3], v[2:3]
	v_pk_mov_b32 v[58:59], v[2:3], v[2:3]
	v_pk_mov_b32 v[60:61], v[2:3], v[2:3]
	v_pk_mov_b32 v[62:63], v[2:3], v[2:3]
	v_pk_mov_b32 v[64:65], v[2:3], v[2:3]
	v_pk_mov_b32 v[66:67], v[2:3], v[2:3]
	v_pk_mov_b32 v[68:69], v[2:3], v[2:3]
	v_pk_mov_b32 v[70:71], v[2:3], v[2:3]
	v_pk_mov_b32 v[72:73], v[2:3], v[2:3]
	v_pk_mov_b32 v[74:75], v[2:3], v[2:3]
	v_pk_mov_b32 v[76:77], v[2:3], v[2:3]
	v_pk_mov_b32 v[78:79], v[2:3], v[2:3]
	v_pk_mov_b32 v[80:81], v[2:3], v[2:3]
	v_pk_mov_b32 v[82:83], v[2:3], v[2:3]
	v_pk_mov_b32 v[84:85], v[2:3], v[2:3]
	v_pk_mov_b32 v[86:87], v[2:3], v[2:3]
	v_pk_mov_b32 v[88:89], v[2:3], v[2:3]
	v_pk_mov_b32 v[90:91], v[2:3], v[2:3]
	v_pk_mov_b32 v[92:93], v[2:3], v[2:3]
	v_pk_mov_b32 v[94:95], v[2:3], v[2:3]
	v_pk_mov_b32 v[96:97], v[2:3], v[2:3]
	v_pk_mov_b32 v[98:99], v[2:3], v[2:3]
	v_pk_mov_b32 v[100:101], v[2:3], v[2:3]
	v_pk_mov_b32 v[102:103], v[2:3], v[2:3]
	v_pk_mov_b32 v[104:105], v[2:3], v[2:3]
	v_pk_mov_b32 v[106:107], v[2:3], v[2:3]
	v_pk_mov_b32 v[108:109], v[2:3], v[2:3]
	v_pk_mov_b32 v[110:111], v[2:3], v[2:3]
	v_pk_mov_b32 v[112:113], v[2:3], v[2:3]
	v_pk_mov_b32 v[114:115], v[2:3], v[2:3]
	v_pk_mov_b32 v[116:117], v[2:3], v[2:3]
	v_pk_mov_b32 v[118:119], v[2:3], v[2:3]
	v_pk_mov_b32 v[120:121], v[2:3], v[2:3]
	v_pk_mov_b32 v[122:123], v[2:3], v[2:3]
	v_pk_mov_b32 v[124:125], v[2:3], v[2:3]
	v_pk_mov_b32 v[126:127], v[2:3], v[2:3]
	v_pk_mov_b32 v[128:129], v[2:3], v[2:3]

.LBB0_1178:
	v_mov_b32_e32 v123, 0
	s_andn2_b64 vcc, exec, s[10:11]
	v_mov_b32_e32 v122, v123
	v_pk_mov_b32 v[0:1], v[122:123], v[122:123]
	v_pk_mov_b32 v[2:3], v[122:123], v[122:123]
	v_pk_mov_b32 v[4:5], v[122:123], v[122:123]
	v_pk_mov_b32 v[6:7], v[122:123], v[122:123]
	v_pk_mov_b32 v[8:9], v[122:123], v[122:123]
	v_pk_mov_b32 v[10:11], v[122:123], v[122:123]
	v_pk_mov_b32 v[12:13], v[122:123], v[122:123]
	v_pk_mov_b32 v[14:15], v[122:123], v[122:123]
	v_pk_mov_b32 v[16:17], v[122:123], v[122:123]
	v_pk_mov_b32 v[18:19], v[122:123], v[122:123]
	v_pk_mov_b32 v[20:21], v[122:123], v[122:123]
	v_pk_mov_b32 v[22:23], v[122:123], v[122:123]
	v_pk_mov_b32 v[24:25], v[122:123], v[122:123]
	v_pk_mov_b32 v[26:27], v[122:123], v[122:123]
	v_pk_mov_b32 v[28:29], v[122:123], v[122:123]
	v_pk_mov_b32 v[30:31], v[122:123], v[122:123]
	v_pk_mov_b32 v[32:33], v[122:123], v[122:123]
	v_pk_mov_b32 v[34:35], v[122:123], v[122:123]
	v_pk_mov_b32 v[36:37], v[122:123], v[122:123]
	v_pk_mov_b32 v[38:39], v[122:123], v[122:123]
	v_pk_mov_b32 v[40:41], v[122:123], v[122:123]
	v_pk_mov_b32 v[42:43], v[122:123], v[122:123]
	v_pk_mov_b32 v[44:45], v[122:123], v[122:123]
	v_pk_mov_b32 v[46:47], v[122:123], v[122:123]
	v_pk_mov_b32 v[48:49], v[122:123], v[122:123]
	v_pk_mov_b32 v[50:51], v[122:123], v[122:123]
	v_pk_mov_b32 v[52:53], v[122:123], v[122:123]
	v_pk_mov_b32 v[54:55], v[122:123], v[122:123]
	v_pk_mov_b32 v[56:57], v[122:123], v[122:123]
	v_pk_mov_b32 v[58:59], v[122:123], v[122:123]
	v_pk_mov_b32 v[60:61], v[122:123], v[122:123]
	v_pk_mov_b32 v[62:63], v[122:123], v[122:123]
	v_pk_mov_b32 v[64:65], v[122:123], v[122:123]
	v_pk_mov_b32 v[66:67], v[122:123], v[122:123]
	v_pk_mov_b32 v[68:69], v[122:123], v[122:123]
	v_pk_mov_b32 v[70:71], v[122:123], v[122:123]
	v_pk_mov_b32 v[72:73], v[122:123], v[122:123]
	v_pk_mov_b32 v[74:75], v[122:123], v[122:123]
	v_pk_mov_b32 v[76:77], v[122:123], v[122:123]
	v_pk_mov_b32 v[78:79], v[122:123], v[122:123]
	v_pk_mov_b32 v[80:81], v[122:123], v[122:123]
	v_pk_mov_b32 v[82:83], v[122:123], v[122:123]
	v_pk_mov_b32 v[84:85], v[122:123], v[122:123]
	v_pk_mov_b32 v[86:87], v[122:123], v[122:123]
	v_pk_mov_b32 v[88:89], v[122:123], v[122:123]
	v_pk_mov_b32 v[90:91], v[122:123], v[122:123]
	v_pk_mov_b32 v[92:93], v[122:123], v[122:123]
	v_pk_mov_b32 v[94:95], v[122:123], v[122:123]
	v_pk_mov_b32 v[96:97], v[122:123], v[122:123]
	v_pk_mov_b32 v[98:99], v[122:123], v[122:123]
	v_pk_mov_b32 v[100:101], v[122:123], v[122:123]
	v_pk_mov_b32 v[102:103], v[122:123], v[122:123]
	v_pk_mov_b32 v[104:105], v[122:123], v[122:123]
	v_pk_mov_b32 v[106:107], v[122:123], v[122:123]
	v_pk_mov_b32 v[108:109], v[122:123], v[122:123]
	v_pk_mov_b32 v[110:111], v[122:123], v[122:123]
	v_pk_mov_b32 v[112:113], v[122:123], v[122:123]
	v_pk_mov_b32 v[114:115], v[122:123], v[122:123]
	v_pk_mov_b32 v[116:117], v[122:123], v[122:123]
	v_pk_mov_b32 v[118:119], v[122:123], v[122:123]
	v_pk_mov_b32 v[120:121], v[122:123], v[122:123]
	v_pk_mov_b32 v[124:125], v[122:123], v[122:123]
	v_pk_mov_b32 v[126:127], v[122:123], v[122:123]
	s_cbranch_vccnz .LBB0_1181
	s_add_u32 s22, s22, 0xe0080
	s_addc_u32 s23, s23, 0
	s_add_u32 s68, s24, 0x100
	v_mov_b32_e32 v0, 0
	s_addc_u32 s69, s25, 0
	s_mov_b32 s24, 0
	v_mov_b32_e32 v1, v0
	v_pk_mov_b32 v[2:3], v[0:1], v[0:1]
	v_pk_mov_b32 v[4:5], v[0:1], v[0:1]
	v_pk_mov_b32 v[6:7], v[0:1], v[0:1]
	v_pk_mov_b32 v[8:9], v[0:1], v[0:1]
	v_pk_mov_b32 v[10:11], v[0:1], v[0:1]
	v_pk_mov_b32 v[12:13], v[0:1], v[0:1]
	v_pk_mov_b32 v[14:15], v[0:1], v[0:1]
	v_pk_mov_b32 v[16:17], v[0:1], v[0:1]
	v_pk_mov_b32 v[18:19], v[0:1], v[0:1]
	v_pk_mov_b32 v[20:21], v[0:1], v[0:1]
	v_pk_mov_b32 v[22:23], v[0:1], v[0:1]
	v_pk_mov_b32 v[24:25], v[0:1], v[0:1]
	v_pk_mov_b32 v[26:27], v[0:1], v[0:1]
	v_pk_mov_b32 v[28:29], v[0:1], v[0:1]
	v_pk_mov_b32 v[30:31], v[0:1], v[0:1]
	v_pk_mov_b32 v[32:33], v[0:1], v[0:1]
	v_pk_mov_b32 v[34:35], v[0:1], v[0:1]
	v_pk_mov_b32 v[36:37], v[0:1], v[0:1]
	v_pk_mov_b32 v[38:39], v[0:1], v[0:1]
	v_pk_mov_b32 v[40:41], v[0:1], v[0:1]
	v_pk_mov_b32 v[42:43], v[0:1], v[0:1]
	v_pk_mov_b32 v[44:45], v[0:1], v[0:1]
	v_pk_mov_b32 v[46:47], v[0:1], v[0:1]
	v_pk_mov_b32 v[48:49], v[0:1], v[0:1]
	v_pk_mov_b32 v[50:51], v[0:1], v[0:1]
	v_pk_mov_b32 v[52:53], v[0:1], v[0:1]
	v_pk_mov_b32 v[54:55], v[0:1], v[0:1]
	v_pk_mov_b32 v[56:57], v[0:1], v[0:1]
	v_pk_mov_b32 v[58:59], v[0:1], v[0:1]
	v_pk_mov_b32 v[60:61], v[0:1], v[0:1]
	v_pk_mov_b32 v[62:63], v[0:1], v[0:1]
	v_pk_mov_b32 v[64:65], v[0:1], v[0:1]
	v_pk_mov_b32 v[66:67], v[0:1], v[0:1]
	v_pk_mov_b32 v[68:69], v[0:1], v[0:1]
	v_pk_mov_b32 v[70:71], v[0:1], v[0:1]
	v_pk_mov_b32 v[72:73], v[0:1], v[0:1]
	v_pk_mov_b32 v[74:75], v[0:1], v[0:1]
	v_pk_mov_b32 v[76:77], v[0:1], v[0:1]
	v_pk_mov_b32 v[78:79], v[0:1], v[0:1]
	v_pk_mov_b32 v[80:81], v[0:1], v[0:1]
	v_pk_mov_b32 v[82:83], v[0:1], v[0:1]
	v_pk_mov_b32 v[84:85], v[0:1], v[0:1]
	v_pk_mov_b32 v[86:87], v[0:1], v[0:1]
	v_pk_mov_b32 v[88:89], v[0:1], v[0:1]
	v_pk_mov_b32 v[90:91], v[0:1], v[0:1]
	v_pk_mov_b32 v[92:93], v[0:1], v[0:1]
	v_pk_mov_b32 v[94:95], v[0:1], v[0:1]
	v_pk_mov_b32 v[96:97], v[0:1], v[0:1]
	v_pk_mov_b32 v[98:99], v[0:1], v[0:1]
	v_pk_mov_b32 v[100:101], v[0:1], v[0:1]
	v_pk_mov_b32 v[102:103], v[0:1], v[0:1]
	v_pk_mov_b32 v[104:105], v[0:1], v[0:1]
	v_pk_mov_b32 v[106:107], v[0:1], v[0:1]
	v_pk_mov_b32 v[108:109], v[0:1], v[0:1]
	v_pk_mov_b32 v[110:111], v[0:1], v[0:1]
	v_pk_mov_b32 v[112:113], v[0:1], v[0:1]
	v_pk_mov_b32 v[114:115], v[0:1], v[0:1]
	v_pk_mov_b32 v[116:117], v[0:1], v[0:1]
	v_pk_mov_b32 v[118:119], v[0:1], v[0:1]
	v_pk_mov_b32 v[120:121], v[0:1], v[0:1]
	v_pk_mov_b32 v[122:123], v[0:1], v[0:1]
	v_pk_mov_b32 v[124:125], v[0:1], v[0:1]
	v_pk_mov_b32 v[126:127], v[0:1], v[0:1]
